# hazard pads behind the QK MFMA chains and behind the fp8 K-loops trimmed to the required distances
# speedup vs baseline: 1.0239x; 1.0089x over previous
.LBB0_265:
	s_or_b64 exec, exec, s[2:3]
	s_nop 11
	v_cndmask_b32_e64 v2, 0, 1, s[20:21]
	v_cmp_ne_u32_e64 s[40:41], 1, v2
	s_andn2_b64 vcc, exec, s[20:21]
	s_cbranch_vccnz .LBB0_267
	s_lshl_b32 s2, s16, 8
	s_ashr_i32 s3, s2, 31
	v_mov_b32_e32 v2, v0
	s_lshl_b64 s[2:3], s[2:3], 2
	s_add_u32 s2, s17, s2
	v_lshlrev_b32_e32 v6, 1, v2
	s_addc_u32 s3, s18, s3
	v_and_b32_e32 v2, 0x180, v6
	v_lshl_add_u64 v[4:5], s[2:3], 0, v[2:3]
	v_and_b32_e32 v2, 0x60, v6
	v_lshl_add_u64 v[4:5], v[4:5], 0, v[2:3]
	global_load_dwordx4 v[36:39], v[4:5], off offset:16
	global_load_dwordx4 v[40:43], v[4:5], off
	global_load_dwordx4 v[44:47], v[4:5], off offset:528
	global_load_dwordx4 v[48:51], v[4:5], off offset:512

.LBB0_452:
	s_nop 0
	v_max3_f32 v2, v70, v71, v72
	v_max3_f32 v4, v73, v74, v75
	v_max3_f32 v5, v76, v77, v78
	v_max3_f32 v175, v79, v80, v81
	v_max3_f32 v2, v2, v4, v5
	v_max3_f32 v4, v82, v83, v84
	v_max3_f32 v2, v2, v175, v4
	v_max_f32_e32 v2, v2, v85
	v_mov_b32_e32 v4, v2
	s_nop 1
	v_permlane32_swap_b32_e32 v2, v4
	v_max_f32_e32 v2, v2, v4
	v_sub_f32_e32 v4, v2, v168
	v_cmp_ge_f32_e32 vcc, s76, v4
	s_cmp_eq_u64 vcc, exec
	s_cbranch_scc1 .LBB0_454
	v_max_f32_e32 v2, v2, v2
	v_max_f32_e32 v4, v168, v168
	v_max_f32_e32 v4, v4, v2
	v_sub_f32_e32 v2, v168, v4
	v_mul_f32_e32 v2, 0x3fb8aa3b, v2
	v_exp_f32_e32 v2, v2
	v_mov_b32_e32 v168, v4
	v_mul_f32_e32 v167, v167, v2
	v_pk_mul_f32 v[68:69], v[68:69], v[2:3] op_sel_hi:[1,0]
	v_pk_mul_f32 v[66:67], v[66:67], v[2:3] op_sel_hi:[1,0]
	v_pk_mul_f32 v[64:65], v[64:65], v[2:3] op_sel_hi:[1,0]
	v_pk_mul_f32 v[62:63], v[62:63], v[2:3] op_sel_hi:[1,0]
	v_pk_mul_f32 v[60:61], v[60:61], v[2:3] op_sel_hi:[1,0]
	v_pk_mul_f32 v[58:59], v[58:59], v[2:3] op_sel_hi:[1,0]
	v_pk_mul_f32 v[56:57], v[56:57], v[2:3] op_sel_hi:[1,0]
	v_pk_mul_f32 v[54:55], v[54:55], v[2:3] op_sel_hi:[1,0]
	v_pk_mul_f32 v[52:53], v[52:53], v[2:3] op_sel_hi:[1,0]
	v_pk_mul_f32 v[50:51], v[50:51], v[2:3] op_sel_hi:[1,0]
	v_pk_mul_f32 v[48:49], v[48:49], v[2:3] op_sel_hi:[1,0]
	v_pk_mul_f32 v[46:47], v[46:47], v[2:3] op_sel_hi:[1,0]
	v_pk_mul_f32 v[44:45], v[44:45], v[2:3] op_sel_hi:[1,0]
	v_pk_mul_f32 v[42:43], v[42:43], v[2:3] op_sel_hi:[1,0]
	v_pk_mul_f32 v[40:41], v[40:41], v[2:3] op_sel_hi:[1,0]
	v_pk_mul_f32 v[38:39], v[38:39], v[2:3] op_sel_hi:[1,0]
	v_pk_mul_f32 v[36:37], v[36:37], v[2:3] op_sel_hi:[1,0]
	v_pk_mul_f32 v[34:35], v[34:35], v[2:3] op_sel_hi:[1,0]
	v_pk_mul_f32 v[32:33], v[32:33], v[2:3] op_sel_hi:[1,0]
	v_pk_mul_f32 v[30:31], v[30:31], v[2:3] op_sel_hi:[1,0]
	v_pk_mul_f32 v[28:29], v[28:29], v[2:3] op_sel_hi:[1,0]
	v_pk_mul_f32 v[26:27], v[26:27], v[2:3] op_sel_hi:[1,0]
	v_pk_mul_f32 v[24:25], v[24:25], v[2:3] op_sel_hi:[1,0]
	v_pk_mul_f32 v[22:23], v[22:23], v[2:3] op_sel_hi:[1,0]
	v_pk_mul_f32 v[20:21], v[20:21], v[2:3] op_sel_hi:[1,0]
	v_pk_mul_f32 v[18:19], v[18:19], v[2:3] op_sel_hi:[1,0]
	v_pk_mul_f32 v[16:17], v[16:17], v[2:3] op_sel_hi:[1,0]
	v_pk_mul_f32 v[14:15], v[14:15], v[2:3] op_sel_hi:[1,0]
	v_pk_mul_f32 v[12:13], v[12:13], v[2:3] op_sel_hi:[1,0]
	v_pk_mul_f32 v[10:11], v[10:11], v[2:3] op_sel_hi:[1,0]
	v_pk_mul_f32 v[8:9], v[8:9], v[2:3] op_sel_hi:[1,0]
	v_pk_mul_f32 v[6:7], v[6:7], v[2:3] op_sel_hi:[1,0]

.LBB0_458:
	s_nop 0
	v_max3_f32 v2, v70, v71, v72
	v_max3_f32 v4, v73, v74, v75
	v_max3_f32 v5, v76, v77, v78
	v_max3_f32 v169, v79, v80, v81
	v_max3_f32 v2, v2, v4, v5
	v_max3_f32 v4, v82, v83, v84
	v_max3_f32 v2, v2, v169, v4
	v_max_f32_e32 v2, v2, v85
	v_mov_b32_e32 v4, v2
	s_nop 1
	v_permlane32_swap_b32_e32 v2, v4
	v_max_f32_e32 v2, v2, v4
	v_sub_f32_e32 v4, v2, v168
	v_cmp_ge_f32_e32 vcc, s76, v4
	s_cmp_eq_u64 vcc, exec
	s_cbranch_scc1 .LBB0_460
	v_max_f32_e32 v2, v2, v2
	v_max_f32_e32 v4, v168, v168
	v_max_f32_e32 v4, v4, v2
	v_sub_f32_e32 v2, v168, v4
	v_mul_f32_e32 v2, 0x3fb8aa3b, v2
	v_exp_f32_e32 v2, v2
	v_mov_b32_e32 v168, v4
	v_mul_f32_e32 v167, v167, v2
	v_pk_mul_f32 v[68:69], v[68:69], v[2:3] op_sel_hi:[1,0]
	v_pk_mul_f32 v[66:67], v[66:67], v[2:3] op_sel_hi:[1,0]
	v_pk_mul_f32 v[64:65], v[64:65], v[2:3] op_sel_hi:[1,0]
	v_pk_mul_f32 v[62:63], v[62:63], v[2:3] op_sel_hi:[1,0]
	v_pk_mul_f32 v[60:61], v[60:61], v[2:3] op_sel_hi:[1,0]
	v_pk_mul_f32 v[58:59], v[58:59], v[2:3] op_sel_hi:[1,0]
	v_pk_mul_f32 v[56:57], v[56:57], v[2:3] op_sel_hi:[1,0]
	v_pk_mul_f32 v[54:55], v[54:55], v[2:3] op_sel_hi:[1,0]
	v_pk_mul_f32 v[52:53], v[52:53], v[2:3] op_sel_hi:[1,0]
	v_pk_mul_f32 v[50:51], v[50:51], v[2:3] op_sel_hi:[1,0]
	v_pk_mul_f32 v[48:49], v[48:49], v[2:3] op_sel_hi:[1,0]
	v_pk_mul_f32 v[46:47], v[46:47], v[2:3] op_sel_hi:[1,0]
	v_pk_mul_f32 v[44:45], v[44:45], v[2:3] op_sel_hi:[1,0]
	v_pk_mul_f32 v[42:43], v[42:43], v[2:3] op_sel_hi:[1,0]
	v_pk_mul_f32 v[40:41], v[40:41], v[2:3] op_sel_hi:[1,0]
	v_pk_mul_f32 v[38:39], v[38:39], v[2:3] op_sel_hi:[1,0]
	v_pk_mul_f32 v[36:37], v[36:37], v[2:3] op_sel_hi:[1,0]
	v_pk_mul_f32 v[34:35], v[34:35], v[2:3] op_sel_hi:[1,0]
	v_pk_mul_f32 v[32:33], v[32:33], v[2:3] op_sel_hi:[1,0]
	v_pk_mul_f32 v[30:31], v[30:31], v[2:3] op_sel_hi:[1,0]
	v_pk_mul_f32 v[28:29], v[28:29], v[2:3] op_sel_hi:[1,0]
	v_pk_mul_f32 v[26:27], v[26:27], v[2:3] op_sel_hi:[1,0]
	v_pk_mul_f32 v[24:25], v[24:25], v[2:3] op_sel_hi:[1,0]
	v_pk_mul_f32 v[22:23], v[22:23], v[2:3] op_sel_hi:[1,0]
	v_pk_mul_f32 v[20:21], v[20:21], v[2:3] op_sel_hi:[1,0]
	v_pk_mul_f32 v[18:19], v[18:19], v[2:3] op_sel_hi:[1,0]
	v_pk_mul_f32 v[16:17], v[16:17], v[2:3] op_sel_hi:[1,0]
	v_pk_mul_f32 v[14:15], v[14:15], v[2:3] op_sel_hi:[1,0]
	v_pk_mul_f32 v[12:13], v[12:13], v[2:3] op_sel_hi:[1,0]
	v_pk_mul_f32 v[10:11], v[10:11], v[2:3] op_sel_hi:[1,0]
	v_pk_mul_f32 v[8:9], v[8:9], v[2:3] op_sel_hi:[1,0]
	v_pk_mul_f32 v[6:7], v[6:7], v[2:3] op_sel_hi:[1,0]

.LBB0_524:
	s_nop 1
	v_max3_f32 v2, v50, v51, v52
	v_max3_f32 v116, v53, v54, v55
	v_max3_f32 v117, v56, v57, v58
	v_max3_f32 v118, v59, v60, v61
	v_max3_f32 v2, v2, v116, v117
	v_max3_f32 v116, v62, v63, v64
	v_max3_f32 v2, v2, v118, v116
	v_max_f32_e32 v2, v2, v65
	v_mov_b32_e32 v116, v2
	s_nop 1
	v_permlane32_swap_b32_e32 v2, v116
	v_max_f32_e32 v2, v2, v116
	v_sub_f32_e32 v116, v2, v110
	v_cmp_ge_f32_e32 vcc, s76, v116
	s_cmp_eq_u64 vcc, exec
	s_cbranch_scc1 .LBB0_526
	v_max_f32_e32 v2, v2, v2
	v_max_f32_e32 v116, v110, v110
	v_max_f32_e32 v116, v116, v2
	v_sub_f32_e32 v2, v110, v116
	v_mul_f32_e32 v2, 0x3fb8aa3b, v2
	v_exp_f32_e32 v2, v2
	v_mov_b32_e32 v110, v116
	v_mul_f32_e32 v107, v107, v2
	v_pk_mul_f32 v[48:49], v[48:49], v[2:3] op_sel_hi:[1,0]
	v_pk_mul_f32 v[46:47], v[46:47], v[2:3] op_sel_hi:[1,0]
	v_pk_mul_f32 v[44:45], v[44:45], v[2:3] op_sel_hi:[1,0]
	v_pk_mul_f32 v[42:43], v[42:43], v[2:3] op_sel_hi:[1,0]
	v_pk_mul_f32 v[40:41], v[40:41], v[2:3] op_sel_hi:[1,0]
	v_pk_mul_f32 v[38:39], v[38:39], v[2:3] op_sel_hi:[1,0]
	v_pk_mul_f32 v[36:37], v[36:37], v[2:3] op_sel_hi:[1,0]
	v_pk_mul_f32 v[34:35], v[34:35], v[2:3] op_sel_hi:[1,0]
	v_pk_mul_f32 v[32:33], v[32:33], v[2:3] op_sel_hi:[1,0]
	v_pk_mul_f32 v[30:31], v[30:31], v[2:3] op_sel_hi:[1,0]
	v_pk_mul_f32 v[28:29], v[28:29], v[2:3] op_sel_hi:[1,0]
	v_pk_mul_f32 v[26:27], v[26:27], v[2:3] op_sel_hi:[1,0]
	v_pk_mul_f32 v[24:25], v[24:25], v[2:3] op_sel_hi:[1,0]
	v_pk_mul_f32 v[22:23], v[22:23], v[2:3] op_sel_hi:[1,0]
	v_pk_mul_f32 v[20:21], v[20:21], v[2:3] op_sel_hi:[1,0]
	v_pk_mul_f32 v[18:19], v[18:19], v[2:3] op_sel_hi:[1,0]

.LBB0_530:
	s_nop 0
	v_max3_f32 v2, v50, v51, v52
	v_max3_f32 v16, v53, v54, v55
	v_max3_f32 v17, v56, v57, v58
	v_max3_f32 v111, v59, v60, v61
	v_max3_f32 v2, v2, v16, v17
	v_max3_f32 v16, v62, v63, v64
	v_max3_f32 v2, v2, v111, v16
	v_max_f32_e32 v2, v2, v65
	v_mov_b32_e32 v16, v2
	s_nop 1
	v_permlane32_swap_b32_e32 v2, v16
	v_max_f32_e32 v2, v2, v16
	v_sub_f32_e32 v16, v2, v110
	v_cmp_ge_f32_e32 vcc, s76, v16
	s_cmp_eq_u64 vcc, exec
	s_cbranch_scc1 .LBB0_509
	v_max_f32_e32 v2, v2, v2
	v_max_f32_e32 v16, v110, v110
	v_max_f32_e32 v16, v16, v2
	v_sub_f32_e32 v2, v110, v16
	v_mul_f32_e32 v2, 0x3fb8aa3b, v2
	v_exp_f32_e32 v2, v2
	v_mov_b32_e32 v110, v16
	v_mul_f32_e32 v107, v107, v2
	v_pk_mul_f32 v[48:49], v[48:49], v[2:3] op_sel_hi:[1,0]
	v_pk_mul_f32 v[46:47], v[46:47], v[2:3] op_sel_hi:[1,0]
	v_pk_mul_f32 v[44:45], v[44:45], v[2:3] op_sel_hi:[1,0]
	v_pk_mul_f32 v[42:43], v[42:43], v[2:3] op_sel_hi:[1,0]
	v_pk_mul_f32 v[40:41], v[40:41], v[2:3] op_sel_hi:[1,0]
	v_pk_mul_f32 v[38:39], v[38:39], v[2:3] op_sel_hi:[1,0]
	v_pk_mul_f32 v[36:37], v[36:37], v[2:3] op_sel_hi:[1,0]
	v_pk_mul_f32 v[34:35], v[34:35], v[2:3] op_sel_hi:[1,0]
	v_pk_mul_f32 v[32:33], v[32:33], v[2:3] op_sel_hi:[1,0]
	v_pk_mul_f32 v[30:31], v[30:31], v[2:3] op_sel_hi:[1,0]
	v_pk_mul_f32 v[28:29], v[28:29], v[2:3] op_sel_hi:[1,0]
	v_pk_mul_f32 v[26:27], v[26:27], v[2:3] op_sel_hi:[1,0]
	v_pk_mul_f32 v[24:25], v[24:25], v[2:3] op_sel_hi:[1,0]
	v_pk_mul_f32 v[22:23], v[22:23], v[2:3] op_sel_hi:[1,0]
	v_pk_mul_f32 v[20:21], v[20:21], v[2:3] op_sel_hi:[1,0]
	v_pk_mul_f32 v[18:19], v[18:19], v[2:3] op_sel_hi:[1,0]
	s_branch .LBB0_509

.LBB0_687:
	s_nop 0
	v_max3_f32 v2, v82, v83, v84
	v_max3_f32 v164, v85, v86, v87
	v_max3_f32 v165, v88, v89, v90
	v_max3_f32 v166, v91, v92, v93
	v_max3_f32 v2, v2, v164, v165
	v_max3_f32 v164, v94, v95, v96
	v_max3_f32 v2, v2, v166, v164
	v_max_f32_e32 v2, v2, v97
	v_mov_b32_e32 v164, v2
	s_nop 1
	v_permlane32_swap_b32_e32 v2, v164
	v_max_f32_e32 v2, v2, v164
	v_sub_f32_e32 v164, v2, v158
	v_cmp_ge_f32_e32 vcc, s76, v164
	s_cmp_eq_u64 vcc, exec
	s_cbranch_scc1 .LBB0_689
	v_max_f32_e32 v2, v2, v2
	v_max_f32_e32 v164, v158, v158
	v_max_f32_e32 v164, v164, v2
	v_sub_f32_e32 v2, v158, v164
	v_mul_f32_e32 v2, 0x3fb8aa3b, v2
	v_exp_f32_e32 v2, v2
	v_mov_b32_e32 v158, v164
	v_mul_f32_e32 v144, v144, v2
	v_pk_mul_f32 v[80:81], v[80:81], v[2:3] op_sel_hi:[1,0]
	v_pk_mul_f32 v[78:79], v[78:79], v[2:3] op_sel_hi:[1,0]
	v_pk_mul_f32 v[76:77], v[76:77], v[2:3] op_sel_hi:[1,0]
	v_pk_mul_f32 v[74:75], v[74:75], v[2:3] op_sel_hi:[1,0]
	v_pk_mul_f32 v[72:73], v[72:73], v[2:3] op_sel_hi:[1,0]
	v_pk_mul_f32 v[70:71], v[70:71], v[2:3] op_sel_hi:[1,0]
	v_pk_mul_f32 v[68:69], v[68:69], v[2:3] op_sel_hi:[1,0]
	v_pk_mul_f32 v[66:67], v[66:67], v[2:3] op_sel_hi:[1,0]
	v_pk_mul_f32 v[64:65], v[64:65], v[2:3] op_sel_hi:[1,0]
	v_pk_mul_f32 v[62:63], v[62:63], v[2:3] op_sel_hi:[1,0]
	v_pk_mul_f32 v[60:61], v[60:61], v[2:3] op_sel_hi:[1,0]
	v_pk_mul_f32 v[58:59], v[58:59], v[2:3] op_sel_hi:[1,0]
	v_pk_mul_f32 v[56:57], v[56:57], v[2:3] op_sel_hi:[1,0]
	v_pk_mul_f32 v[54:55], v[54:55], v[2:3] op_sel_hi:[1,0]
	v_pk_mul_f32 v[52:53], v[52:53], v[2:3] op_sel_hi:[1,0]
	v_pk_mul_f32 v[50:51], v[50:51], v[2:3] op_sel_hi:[1,0]

.LBB0_695:
	s_nop 0
	v_max3_f32 v2, v82, v83, v84
	v_max3_f32 v16, v85, v86, v87
	v_max3_f32 v17, v88, v89, v90
	v_max3_f32 v159, v91, v92, v93
	v_max3_f32 v2, v2, v16, v17
	v_max3_f32 v16, v94, v95, v96
	v_max3_f32 v2, v2, v159, v16
	v_max_f32_e32 v2, v2, v97
	v_mov_b32_e32 v16, v2
	s_nop 1
	v_permlane32_swap_b32_e32 v2, v16
	v_max_f32_e32 v2, v2, v16
	v_sub_f32_e32 v16, v2, v158
	v_cmp_ge_f32_e32 vcc, s76, v16
	s_cmp_eq_u64 vcc, exec
	s_cbranch_scc1 .LBB0_668
	v_max_f32_e32 v2, v2, v2
	v_max_f32_e32 v16, v158, v158
	v_max_f32_e32 v16, v16, v2
	v_sub_f32_e32 v2, v158, v16
	v_mul_f32_e32 v2, 0x3fb8aa3b, v2
	v_exp_f32_e32 v2, v2
	v_mov_b32_e32 v158, v16
	v_mul_f32_e32 v144, v144, v2
	v_pk_mul_f32 v[80:81], v[80:81], v[2:3] op_sel_hi:[1,0]
	v_pk_mul_f32 v[78:79], v[78:79], v[2:3] op_sel_hi:[1,0]
	v_pk_mul_f32 v[76:77], v[76:77], v[2:3] op_sel_hi:[1,0]
	v_pk_mul_f32 v[74:75], v[74:75], v[2:3] op_sel_hi:[1,0]
	v_pk_mul_f32 v[72:73], v[72:73], v[2:3] op_sel_hi:[1,0]
	v_pk_mul_f32 v[70:71], v[70:71], v[2:3] op_sel_hi:[1,0]
	v_pk_mul_f32 v[68:69], v[68:69], v[2:3] op_sel_hi:[1,0]
	v_pk_mul_f32 v[66:67], v[66:67], v[2:3] op_sel_hi:[1,0]
	v_pk_mul_f32 v[64:65], v[64:65], v[2:3] op_sel_hi:[1,0]
	v_pk_mul_f32 v[62:63], v[62:63], v[2:3] op_sel_hi:[1,0]
	v_pk_mul_f32 v[60:61], v[60:61], v[2:3] op_sel_hi:[1,0]
	v_pk_mul_f32 v[58:59], v[58:59], v[2:3] op_sel_hi:[1,0]
	v_pk_mul_f32 v[56:57], v[56:57], v[2:3] op_sel_hi:[1,0]
	v_pk_mul_f32 v[54:55], v[54:55], v[2:3] op_sel_hi:[1,0]
	v_pk_mul_f32 v[52:53], v[52:53], v[2:3] op_sel_hi:[1,0]
	v_pk_mul_f32 v[50:51], v[50:51], v[2:3] op_sel_hi:[1,0]
	s_branch .LBB0_668

.LBB0_785:
	s_nop 1
	v_max3_f32 v2, v50, v51, v52
	v_max3_f32 v119, v53, v54, v55
	v_max3_f32 v120, v56, v57, v58
	v_max3_f32 v121, v59, v60, v61
	v_max3_f32 v2, v2, v119, v120
	v_max3_f32 v119, v62, v63, v64
	v_max3_f32 v2, v2, v121, v119
	v_max_f32_e32 v2, v2, v65
	v_mov_b32_e32 v119, v2
	s_nop 1
	v_permlane32_swap_b32_e32 v2, v119
	v_max_f32_e32 v2, v2, v119
	v_sub_f32_e32 v119, v2, v113
	v_cmp_ge_f32_e32 vcc, s76, v119
	s_cmp_eq_u64 vcc, exec
	s_cbranch_scc1 .LBB0_787
	v_max_f32_e32 v2, v2, v2
	v_max_f32_e32 v119, v113, v113
	v_max_f32_e32 v119, v119, v2
	v_sub_f32_e32 v2, v113, v119
	v_mul_f32_e32 v2, 0x3fb8aa3b, v2
	v_exp_f32_e32 v2, v2
	v_mov_b32_e32 v113, v119
	v_mul_f32_e32 v108, v108, v2
	v_pk_mul_f32 v[48:49], v[48:49], v[2:3] op_sel_hi:[1,0]
	v_pk_mul_f32 v[46:47], v[46:47], v[2:3] op_sel_hi:[1,0]
	v_pk_mul_f32 v[44:45], v[44:45], v[2:3] op_sel_hi:[1,0]
	v_pk_mul_f32 v[42:43], v[42:43], v[2:3] op_sel_hi:[1,0]
	v_pk_mul_f32 v[40:41], v[40:41], v[2:3] op_sel_hi:[1,0]
	v_pk_mul_f32 v[38:39], v[38:39], v[2:3] op_sel_hi:[1,0]
	v_pk_mul_f32 v[36:37], v[36:37], v[2:3] op_sel_hi:[1,0]
	v_pk_mul_f32 v[34:35], v[34:35], v[2:3] op_sel_hi:[1,0]
	v_pk_mul_f32 v[32:33], v[32:33], v[2:3] op_sel_hi:[1,0]
	v_pk_mul_f32 v[30:31], v[30:31], v[2:3] op_sel_hi:[1,0]
	v_pk_mul_f32 v[28:29], v[28:29], v[2:3] op_sel_hi:[1,0]
	v_pk_mul_f32 v[26:27], v[26:27], v[2:3] op_sel_hi:[1,0]
	v_pk_mul_f32 v[24:25], v[24:25], v[2:3] op_sel_hi:[1,0]
	v_pk_mul_f32 v[22:23], v[22:23], v[2:3] op_sel_hi:[1,0]
	v_pk_mul_f32 v[20:21], v[20:21], v[2:3] op_sel_hi:[1,0]
	v_pk_mul_f32 v[18:19], v[18:19], v[2:3] op_sel_hi:[1,0]

.LBB0_791:
	s_nop 0
	v_max3_f32 v2, v50, v51, v52
	v_max3_f32 v16, v53, v54, v55
	v_max3_f32 v17, v56, v57, v58
	v_max3_f32 v114, v59, v60, v61
	v_max3_f32 v2, v2, v16, v17
	v_max3_f32 v16, v62, v63, v64
	v_max3_f32 v2, v2, v114, v16
	v_max_f32_e32 v2, v2, v65
	v_mov_b32_e32 v16, v2
	s_nop 1
	v_permlane32_swap_b32_e32 v2, v16
	v_max_f32_e32 v2, v2, v16
	v_sub_f32_e32 v16, v2, v113
	v_cmp_ge_f32_e32 vcc, s76, v16
	s_cmp_eq_u64 vcc, exec
	s_cbranch_scc1 .LBB0_770
	v_max_f32_e32 v2, v2, v2
	v_max_f32_e32 v16, v113, v113
	v_max_f32_e32 v16, v16, v2
	v_sub_f32_e32 v2, v113, v16
	v_mul_f32_e32 v2, 0x3fb8aa3b, v2
	v_exp_f32_e32 v2, v2
	v_mov_b32_e32 v113, v16
	v_mul_f32_e32 v108, v108, v2
	v_pk_mul_f32 v[48:49], v[48:49], v[2:3] op_sel_hi:[1,0]
	v_pk_mul_f32 v[46:47], v[46:47], v[2:3] op_sel_hi:[1,0]
	v_pk_mul_f32 v[44:45], v[44:45], v[2:3] op_sel_hi:[1,0]
	v_pk_mul_f32 v[42:43], v[42:43], v[2:3] op_sel_hi:[1,0]
	v_pk_mul_f32 v[40:41], v[40:41], v[2:3] op_sel_hi:[1,0]
	v_pk_mul_f32 v[38:39], v[38:39], v[2:3] op_sel_hi:[1,0]
	v_pk_mul_f32 v[36:37], v[36:37], v[2:3] op_sel_hi:[1,0]
	v_pk_mul_f32 v[34:35], v[34:35], v[2:3] op_sel_hi:[1,0]
	v_pk_mul_f32 v[32:33], v[32:33], v[2:3] op_sel_hi:[1,0]
	v_pk_mul_f32 v[30:31], v[30:31], v[2:3] op_sel_hi:[1,0]
	v_pk_mul_f32 v[28:29], v[28:29], v[2:3] op_sel_hi:[1,0]
	v_pk_mul_f32 v[26:27], v[26:27], v[2:3] op_sel_hi:[1,0]
	v_pk_mul_f32 v[24:25], v[24:25], v[2:3] op_sel_hi:[1,0]
	v_pk_mul_f32 v[22:23], v[22:23], v[2:3] op_sel_hi:[1,0]
	v_pk_mul_f32 v[20:21], v[20:21], v[2:3] op_sel_hi:[1,0]
	v_pk_mul_f32 v[18:19], v[18:19], v[2:3] op_sel_hi:[1,0]
	s_branch .LBB0_770

.LBB0_912:
	s_or_b64 exec, exec, s[2:3]
	v_mov_b32_e32 v4, v0
	s_nop 11
	s_lshl_b32 s2, s20, 8
	v_ashrrev_i32_e32 v5, 2, v4
	v_and_b32_e32 v5, 0xffffffc0, v5
	v_lshl_add_u32 v5, s26, 8, v5
	v_and_or_b32 v6, v4, 15, v5
	v_lshrrev_b32_e32 v5, 1, v4
	v_and_b32_e32 v7, 0x60, v5
	v_and_b32_e32 v5, 24, v5
	v_or3_b32 v28, v7, s2, v5
	v_bfe_u32 v7, v4, 4, 1
	v_lshlrev_b32_e32 v8, 4, v7
	v_or_b32_e32 v18, v6, v8
	v_mov_b64_e32 v[4:5], s[8:9]
	v_mad_i64_i32 v[22:23], s[2:3], v18, s70, v[4:5]
	v_or_b32_e32 v4, 32, v8
	v_add_u32_e32 v5, 0x80, v6
	s_mov_b64 s[2:3], -1
	s_and_b64 vcc, exec, s[40:41]
	v_ashrrev_i32_e32 v29, 31, v28
	v_lshlrev_b32_e32 v203, 3, v7
	v_or_b32_e32 v20, v6, v4
	v_or_b32_e32 v32, v5, v8
	v_or_b32_e32 v30, v5, v4
	s_cbranch_vccz .LBB0_915
	v_sub_co_u32_e32 v24, vcc, 0, v203
	v_lshl_add_u64 v[4:5], v[22:23], 0, v[28:29]
	s_nop 0
	v_subb_co_u32_e64 v25, s[2:3], 0, 0, vcc
	v_lshl_add_u64 v[4:5], v[4:5], 0, v[24:25]
	s_mov_b64 s[20:21], 0x2400
	v_lshl_add_u64 v[6:7], v[4:5], 0, s[20:21]
	v_add_co_u32_e32 v4, vcc, 0x2000, v4
	v_mov_b64_e32 v[16:17], s[8:9]
	s_nop 0
	v_addc_co_u32_e32 v5, vcc, 0, v5, vcc
	global_load_dwordx4 v[12:15], v[4:5], off offset:1024
	v_mad_i64_i32 v[4:5], s[2:3], v20, s70, v[16:17]
	v_lshl_add_u64 v[4:5], v[4:5], 0, v[28:29]
	v_lshl_add_u64 v[4:5], v[4:5], 0, v[24:25]
	v_lshl_add_u64 v[26:27], v[4:5], 0, s[20:21]
	v_add_co_u32_e32 v4, vcc, s67, v4
	v_ashrrev_i32_e32 v19, 31, v18
	s_nop 0
	v_addc_co_u32_e32 v5, vcc, 0, v5, vcc
	global_load_dwordx4 v[8:11], v[4:5], off offset:1024
	global_load_dwordx4 v[4:7], v[6:7], off offset:128
	v_lshlrev_b64 v[18:19], 10, v[18:19]
	v_lshl_add_u64 v[18:19], s[10:11], 0, v[18:19]
	v_lshl_add_u64 v[18:19], v[18:19], 0, v[28:29]
	v_lshl_add_u64 v[18:19], v[18:19], 0, v[24:25]
	v_ashrrev_i32_e32 v21, 31, v20
	s_waitcnt vmcnt(0)
	v_permlane16_swap_b32_e32 v12, v14
	v_permlane16_swap_b32_e32 v13, v15
	v_cvt_f32_ubyte0_e32 v31, v12
	v_cvt_f32_ubyte1_e32 v33, v12
	v_cvt_f32_ubyte2_e32 v34, v12
	v_cvt_f32_ubyte3_e32 v12, v12
	v_mul_f32_e32 v31, 0x3b808081, v31
	v_mul_f32_e32 v33, 0x3b808081, v33
	v_mul_f32_e32 v12, 0x3b808081, v12
	v_cvt_f32_ubyte0_e32 v35, v13
	v_cvt_f32_ubyte1_e32 v164, v13
	v_cvt_f32_ubyte2_e32 v165, v13
	v_cvt_f32_ubyte3_e32 v13, v13
	v_mul_f32_e32 v31, v160, v31
	v_mul_f32_e32 v33, v161, v33
	v_mul_f32_e32 v12, v163, v12
	v_mul_f32_e32 v35, 0x3b808081, v35
	v_mul_f32_e32 v164, 0x3b808081, v164
	v_mul_f32_e32 v13, 0x3b808081, v13
	v_mul_f32_e32 v31, 0x41800000, v31
	v_mul_f32_e32 v33, 0x41800000, v33
	v_mul_f32_e32 v12, 0x41800000, v12
	v_mul_f32_e32 v35, v156, v35
	v_mul_f32_e32 v164, v157, v164
	v_mul_f32_e32 v13, v159, v13
	v_med3_f32 v31, v31, s78, v198
	v_med3_f32 v33, v33, s78, v198
	v_med3_f32 v192, v12, s78, v198
	v_mov_b32_e32 v12, v3
	v_mul_f32_e32 v34, 0x3b808081, v34
	v_cvt_pk_fp8_f32 v12, v31, v33
	v_mul_f32_e32 v31, 0x41800000, v35
	v_mul_f32_e32 v33, 0x41800000, v164
	v_mul_f32_e32 v13, 0x41800000, v13
	v_mul_f32_e32 v34, v162, v34
	v_med3_f32 v31, v31, s78, v198
	v_med3_f32 v33, v33, s78, v198
	v_med3_f32 v35, v13, s78, v198
	v_mov_b32_e32 v13, v3
	v_mul_f32_e32 v165, 0x3b808081, v165
	v_mul_f32_e32 v34, 0x41800000, v34
	v_cvt_pk_fp8_f32 v13, v31, v33
	v_mul_f32_e32 v165, v158, v165
	v_med3_f32 v34, v34, s78, v198
	v_cvt_pk_fp8_f32 v12, v34, v192 op_sel:[0,0,1]
	v_mul_f32_e32 v34, 0x41800000, v165
	v_med3_f32 v34, v34, s78, v198
	v_cvt_pk_fp8_f32 v13, v34, v35 op_sel:[0,0,1]
	v_cvt_f32_ubyte0_e32 v31, v14
	v_cvt_f32_ubyte1_e32 v33, v14
	v_cvt_f32_ubyte2_e32 v34, v14
	v_cvt_f32_ubyte3_e32 v14, v14
	v_mul_f32_e32 v31, 0x3b808081, v31
	v_mul_f32_e32 v33, 0x3b808081, v33
	v_mul_f32_e32 v14, 0x3b808081, v14
	v_cvt_f32_ubyte0_e32 v35, v15
	v_cvt_f32_ubyte1_e32 v164, v15
	v_cvt_f32_ubyte2_e32 v165, v15
	v_cvt_f32_ubyte3_e32 v15, v15
	v_mul_f32_e32 v31, v152, v31
	v_mul_f32_e32 v33, v153, v33
	v_mul_f32_e32 v14, v155, v14
	v_mul_f32_e32 v35, 0x3b808081, v35
	v_mul_f32_e32 v164, 0x3b808081, v164
	v_mul_f32_e32 v15, 0x3b808081, v15
	v_mul_f32_e32 v31, 0x41800000, v31
	v_mul_f32_e32 v33, 0x41800000, v33
	v_mul_f32_e32 v14, 0x41800000, v14
	v_mul_f32_e32 v35, v148, v35
	v_mul_f32_e32 v164, v149, v164
	v_mul_f32_e32 v15, v151, v15
	v_med3_f32 v31, v31, s78, v198
	v_med3_f32 v33, v33, s78, v198
	v_med3_f32 v192, v14, s78, v198
	v_mov_b32_e32 v14, v3
	v_mul_f32_e32 v34, 0x3b808081, v34
	v_cvt_pk_fp8_f32 v14, v31, v33
	v_mul_f32_e32 v31, 0x41800000, v35
	v_mul_f32_e32 v33, 0x41800000, v164
	v_mul_f32_e32 v15, 0x41800000, v15
	v_mul_f32_e32 v34, v154, v34
	v_med3_f32 v31, v31, s78, v198
	v_med3_f32 v33, v33, s78, v198
	v_med3_f32 v35, v15, s78, v198
	v_mov_b32_e32 v15, v3
	v_mul_f32_e32 v165, 0x3b808081, v165
	v_mul_f32_e32 v34, 0x41800000, v34
	v_cvt_pk_fp8_f32 v15, v31, v33
	v_mul_f32_e32 v165, v150, v165
	v_med3_f32 v34, v34, s78, v198
	v_cvt_pk_fp8_f32 v14, v34, v192 op_sel:[0,0,1]
	v_mul_f32_e32 v34, 0x41800000, v165
	v_med3_f32 v34, v34, s78, v198
	v_cvt_pk_fp8_f32 v15, v34, v35 op_sel:[0,0,1]
	v_permlane16_swap_b32_e32 v12, v14
	v_permlane16_swap_b32_e32 v8, v10
	v_permlane16_swap_b32_e32 v13, v15
	global_store_dwordx4 v[18:19], v[12:15], off
	global_load_dwordx4 v[12:15], v[26:27], off offset:128
	v_permlane16_swap_b32_e32 v9, v11
	v_cvt_f32_ubyte0_e32 v26, v8
	v_cvt_f32_ubyte1_e32 v27, v8
	v_cvt_f32_ubyte2_e32 v31, v8
	v_cvt_f32_ubyte3_e32 v8, v8
	v_mul_f32_e32 v26, 0x3b808081, v26
	v_mul_f32_e32 v27, 0x3b808081, v27
	v_mul_f32_e32 v8, 0x3b808081, v8
	v_cvt_f32_ubyte0_e32 v33, v9
	v_cvt_f32_ubyte1_e32 v34, v9
	v_cvt_f32_ubyte2_e32 v35, v9
	v_cvt_f32_ubyte3_e32 v9, v9
	v_mul_f32_e32 v26, v144, v26
	v_mul_f32_e32 v27, v145, v27
	v_mul_f32_e32 v8, v147, v8
	v_mul_f32_e32 v33, 0x3b808081, v33
	v_mul_f32_e32 v34, 0x3b808081, v34
	v_mul_f32_e32 v9, 0x3b808081, v9
	v_mul_f32_e32 v26, 0x41800000, v26
	v_mul_f32_e32 v27, 0x41800000, v27
	v_mul_f32_e32 v8, 0x41800000, v8
	v_mul_f32_e32 v33, v140, v33
	v_mul_f32_e32 v34, v141, v34
	v_mul_f32_e32 v9, v143, v9
	v_med3_f32 v26, v26, s78, v198
	v_med3_f32 v27, v27, s78, v198
	v_med3_f32 v164, v8, s78, v198
	v_mov_b32_e32 v8, v3
	v_mul_f32_e32 v31, 0x3b808081, v31
	v_cvt_pk_fp8_f32 v8, v26, v27
	v_mul_f32_e32 v26, 0x41800000, v33
	v_mul_f32_e32 v27, 0x41800000, v34
	v_mul_f32_e32 v9, 0x41800000, v9
	v_mul_f32_e32 v31, v146, v31
	v_med3_f32 v26, v26, s78, v198
	v_med3_f32 v27, v27, s78, v198
	v_med3_f32 v33, v9, s78, v198
	v_mov_b32_e32 v9, v3
	v_mul_f32_e32 v35, 0x3b808081, v35
	v_mul_f32_e32 v31, 0x41800000, v31
	v_cvt_pk_fp8_f32 v9, v26, v27
	v_mul_f32_e32 v35, v142, v35
	v_med3_f32 v31, v31, s78, v198
	v_cvt_pk_fp8_f32 v8, v31, v164 op_sel:[0,0,1]
	v_mul_f32_e32 v31, 0x41800000, v35
	v_med3_f32 v31, v31, s78, v198
	v_cvt_pk_fp8_f32 v9, v31, v33 op_sel:[0,0,1]
	v_cvt_f32_ubyte0_e32 v26, v10
	v_cvt_f32_ubyte1_e32 v27, v10
	v_cvt_f32_ubyte2_e32 v31, v10
	v_cvt_f32_ubyte3_e32 v10, v10
	v_mul_f32_e32 v26, 0x3b808081, v26
	v_mul_f32_e32 v27, 0x3b808081, v27
	v_mul_f32_e32 v10, 0x3b808081, v10
	v_cvt_f32_ubyte0_e32 v33, v11
	v_cvt_f32_ubyte1_e32 v34, v11
	v_cvt_f32_ubyte2_e32 v35, v11
	v_cvt_f32_ubyte3_e32 v11, v11
	v_mul_f32_e32 v26, v136, v26
	v_mul_f32_e32 v27, v137, v27
	v_mul_f32_e32 v10, v139, v10
	v_mul_f32_e32 v33, 0x3b808081, v33
	v_mul_f32_e32 v34, 0x3b808081, v34
	v_mul_f32_e32 v11, 0x3b808081, v11
	v_mul_f32_e32 v26, 0x41800000, v26
	v_mul_f32_e32 v27, 0x41800000, v27
	v_mul_f32_e32 v10, 0x41800000, v10
	v_mul_f32_e32 v33, v132, v33
	v_mul_f32_e32 v34, v133, v34
	v_mul_f32_e32 v11, v135, v11
	v_med3_f32 v26, v26, s78, v198
	v_med3_f32 v27, v27, s78, v198
	v_med3_f32 v164, v10, s78, v198
	v_mov_b32_e32 v10, v3
	v_mul_f32_e32 v31, 0x3b808081, v31
	v_cvt_pk_fp8_f32 v10, v26, v27
	v_mul_f32_e32 v26, 0x41800000, v33
	v_mul_f32_e32 v27, 0x41800000, v34
	v_mul_f32_e32 v11, 0x41800000, v11
	v_mul_f32_e32 v31, v138, v31
	v_med3_f32 v26, v26, s78, v198
	v_med3_f32 v27, v27, s78, v198
	v_med3_f32 v33, v11, s78, v198
	v_mov_b32_e32 v11, v3
	v_mul_f32_e32 v35, 0x3b808081, v35
	v_mul_f32_e32 v31, 0x41800000, v31
	v_cvt_pk_fp8_f32 v11, v26, v27
	v_mul_f32_e32 v35, v134, v35
	v_med3_f32 v31, v31, s78, v198
	v_cvt_pk_fp8_f32 v10, v31, v164 op_sel:[0,0,1]
	v_mul_f32_e32 v31, 0x41800000, v35
	v_med3_f32 v31, v31, s78, v198
	v_cvt_pk_fp8_f32 v11, v31, v33 op_sel:[0,0,1]
	v_lshlrev_b64 v[26:27], 10, v[20:21]
	v_lshl_add_u64 v[26:27], s[10:11], 0, v[26:27]
	v_lshl_add_u64 v[26:27], v[26:27], 0, v[28:29]
	v_permlane16_swap_b32_e32 v8, v10
	v_permlane16_swap_b32_e32 v9, v11
	v_lshl_add_u64 v[26:27], v[26:27], 0, v[24:25]
	global_store_dwordx4 v[26:27], v[8:11], off
	v_permlane16_swap_b32_e32 v4, v6
	s_nop 0
	v_mad_i64_i32 v[8:9], s[2:3], v32, s70, v[16:17]
	v_lshl_add_u64 v[8:9], v[8:9], 0, v[28:29]
	v_lshl_add_u64 v[8:9], v[8:9], 0, v[24:25]
	v_lshl_add_u64 v[34:35], v[8:9], 0, s[20:21]
	v_add_co_u32_e32 v8, vcc, s67, v8
	v_permlane16_swap_b32_e32 v5, v7
	s_nop 0
	v_addc_co_u32_e32 v9, vcc, 0, v9, vcc
	global_load_dwordx4 v[8:11], v[8:9], off offset:1024
	v_cvt_f32_ubyte0_e32 v21, v4
	v_cvt_f32_ubyte1_e32 v31, v4
	v_cvt_f32_ubyte2_e32 v164, v4
	v_cvt_f32_ubyte3_e32 v4, v4
	v_mul_f32_e32 v21, 0x3b808081, v21
	v_mul_f32_e32 v31, 0x3b808081, v31
	v_mul_f32_e32 v4, 0x3b808081, v4
	v_cvt_f32_ubyte0_e32 v165, v5
	v_cvt_f32_ubyte1_e32 v192, v5
	v_cvt_f32_ubyte2_e32 v193, v5
	v_cvt_f32_ubyte3_e32 v5, v5
	v_mul_f32_e32 v21, v128, v21
	v_mul_f32_e32 v31, v129, v31
	v_mul_f32_e32 v4, v131, v4
	v_mul_f32_e32 v165, 0x3b808081, v165
	v_mul_f32_e32 v192, 0x3b808081, v192
	v_mul_f32_e32 v5, 0x3b808081, v5
	v_mul_f32_e32 v21, 0x41800000, v21
	v_mul_f32_e32 v31, 0x41800000, v31
	v_mul_f32_e32 v4, 0x41800000, v4
	v_mul_f32_e32 v165, v124, v165
	v_mul_f32_e32 v192, v125, v192
	v_mul_f32_e32 v5, v127, v5
	v_med3_f32 v21, v21, s78, v198
	v_med3_f32 v31, v31, s78, v198
	v_med3_f32 v194, v4, s78, v198
	v_mov_b32_e32 v4, v3
	v_mul_f32_e32 v164, 0x3b808081, v164
	v_cvt_pk_fp8_f32 v4, v21, v31
	v_mul_f32_e32 v21, 0x41800000, v165
	v_mul_f32_e32 v31, 0x41800000, v192
	v_mul_f32_e32 v5, 0x41800000, v5
	v_mul_f32_e32 v164, v130, v164
	v_med3_f32 v21, v21, s78, v198
	v_med3_f32 v31, v31, s78, v198
	v_med3_f32 v165, v5, s78, v198
	v_mov_b32_e32 v5, v3
	v_mul_f32_e32 v193, 0x3b808081, v193
	v_mul_f32_e32 v164, 0x41800000, v164
	v_cvt_pk_fp8_f32 v5, v21, v31
	v_mul_f32_e32 v193, v126, v193
	v_med3_f32 v164, v164, s78, v198
	v_cvt_pk_fp8_f32 v4, v164, v194 op_sel:[0,0,1]
	v_mul_f32_e32 v164, 0x41800000, v193
	v_med3_f32 v164, v164, s78, v198
	v_cvt_pk_fp8_f32 v5, v164, v165 op_sel:[0,0,1]
	v_cvt_f32_ubyte0_e32 v21, v6
	v_cvt_f32_ubyte1_e32 v31, v6
	v_cvt_f32_ubyte2_e32 v164, v6
	v_cvt_f32_ubyte3_e32 v6, v6
	v_mul_f32_e32 v21, 0x3b808081, v21
	v_mul_f32_e32 v31, 0x3b808081, v31
	v_mul_f32_e32 v6, 0x3b808081, v6
	v_cvt_f32_ubyte0_e32 v165, v7
	v_cvt_f32_ubyte1_e32 v192, v7
	v_cvt_f32_ubyte2_e32 v193, v7
	v_cvt_f32_ubyte3_e32 v7, v7
	v_mul_f32_e32 v21, v120, v21
	v_mul_f32_e32 v31, v121, v31
	v_mul_f32_e32 v6, v123, v6
	v_mul_f32_e32 v165, 0x3b808081, v165
	v_mul_f32_e32 v192, 0x3b808081, v192
	v_mul_f32_e32 v7, 0x3b808081, v7
	v_mul_f32_e32 v21, 0x41800000, v21
	v_mul_f32_e32 v31, 0x41800000, v31
	v_mul_f32_e32 v6, 0x41800000, v6
	v_mul_f32_e32 v165, v116, v165
	v_mul_f32_e32 v192, v117, v192
	v_mul_f32_e32 v7, v119, v7
	v_med3_f32 v21, v21, s78, v198
	v_med3_f32 v31, v31, s78, v198
	v_med3_f32 v194, v6, s78, v198
	v_mov_b32_e32 v6, v3
	v_mul_f32_e32 v164, 0x3b808081, v164
	v_cvt_pk_fp8_f32 v6, v21, v31
	v_mul_f32_e32 v21, 0x41800000, v165
	v_mul_f32_e32 v31, 0x41800000, v192
	v_mul_f32_e32 v7, 0x41800000, v7
	v_mul_f32_e32 v164, v122, v164
	v_med3_f32 v21, v21, s78, v198
	v_med3_f32 v31, v31, s78, v198
	v_med3_f32 v165, v7, s78, v198
	v_mov_b32_e32 v7, v3
	v_mul_f32_e32 v193, 0x3b808081, v193
	v_mul_f32_e32 v164, 0x41800000, v164
	v_cvt_pk_fp8_f32 v7, v21, v31
	v_mul_f32_e32 v193, v118, v193
	v_med3_f32 v164, v164, s78, v198
	v_cvt_pk_fp8_f32 v6, v164, v194 op_sel:[0,0,1]
	v_mul_f32_e32 v164, 0x41800000, v193
	v_med3_f32 v164, v164, s78, v198
	v_cvt_pk_fp8_f32 v7, v164, v165 op_sel:[0,0,1]
	v_permlane16_swap_b32_e32 v4, v6
	s_waitcnt vmcnt(0)
	v_permlane16_swap_b32_e32 v8, v10
	v_permlane16_swap_b32_e32 v5, v7
	global_store_dwordx4 v[18:19], v[4:7], off offset:128
	v_permlane16_swap_b32_e32 v9, v11
	s_nop 0
	v_mad_i64_i32 v[4:5], s[2:3], v30, s70, v[16:17]
	v_lshl_add_u64 v[4:5], v[4:5], 0, v[28:29]
	v_lshl_add_u64 v[4:5], v[4:5], 0, v[24:25]
	v_lshl_add_u64 v[164:165], v[4:5], 0, s[20:21]
	v_add_co_u32_e32 v4, vcc, s67, v4
	v_mov_b32_e32 v6, v14
	s_nop 0
	v_addc_co_u32_e32 v5, vcc, 0, v5, vcc
	v_permlane16_swap_b32_e32 v12, v6
	global_load_dwordx4 v[16:19], v[4:5], off offset:1024
	v_cvt_f32_ubyte0_e32 v4, v12
	v_cvt_f32_ubyte1_e32 v5, v12
	v_mul_f32_e32 v4, 0x3b808081, v4
	v_mov_b32_e32 v7, v15
	v_cvt_f32_ubyte2_e32 v14, v12
	v_mul_f32_e32 v5, 0x3b808081, v5
	v_mul_f32_e32 v4, v112, v4
	v_permlane16_swap_b32_e32 v13, v7
	v_cvt_f32_ubyte3_e32 v12, v12
	v_mul_f32_e32 v14, 0x3b808081, v14
	v_mul_f32_e32 v5, v113, v5
	v_mul_f32_e32 v4, 0x41800000, v4
	v_mul_f32_e32 v12, 0x3b808081, v12
	v_mul_f32_e32 v14, v114, v14
	v_med3_f32 v193, v4, s78, v198
	v_mul_f32_e32 v4, 0x41800000, v5
	v_mul_f32_e32 v12, v115, v12
	v_med3_f32 v5, v4, s78, v198
	v_mul_f32_e32 v4, 0x41800000, v14
	v_med3_f32 v14, v4, s78, v198
	v_mul_f32_e32 v4, 0x41800000, v12
	v_med3_f32 v12, v4, s78, v198
	v_mov_b32_e32 v4, v3
	v_cvt_f32_ubyte0_e32 v15, v13
	v_cvt_pk_fp8_f32 v4, v193, v5
	v_cvt_f32_ubyte1_e32 v21, v13
	v_mul_f32_e32 v15, 0x3b808081, v15
	v_cvt_f32_ubyte2_e32 v192, v13
	v_mul_f32_e32 v21, 0x3b808081, v21
	v_mul_f32_e32 v15, v108, v15
	v_cvt_f32_ubyte3_e32 v13, v13
	v_mul_f32_e32 v192, 0x3b808081, v192
	v_mul_f32_e32 v21, v109, v21
	v_mul_f32_e32 v5, 0x41800000, v15
	v_mul_f32_e32 v13, 0x3b808081, v13
	v_mul_f32_e32 v192, v110, v192
	v_cvt_pk_fp8_f32 v4, v14, v12 op_sel:[0,0,1]
	v_med3_f32 v12, v5, s78, v198
	v_mul_f32_e32 v5, 0x41800000, v21
	v_mul_f32_e32 v13, v111, v13
	v_med3_f32 v14, v5, s78, v198
	v_mul_f32_e32 v5, 0x41800000, v192
	v_med3_f32 v15, v5, s78, v198
	v_mul_f32_e32 v5, 0x41800000, v13
	v_med3_f32 v13, v5, s78, v198
	v_mov_b32_e32 v5, v3
	v_cvt_pk_fp8_f32 v5, v12, v14
	v_cvt_f32_ubyte0_e32 v12, v6
	v_cvt_f32_ubyte2_e32 v14, v6
	v_cvt_pk_fp8_f32 v5, v15, v13 op_sel:[0,0,1]
	v_cvt_f32_ubyte1_e32 v13, v6
	v_cvt_f32_ubyte3_e32 v6, v6
	v_mul_f32_e32 v12, 0x3b808081, v12
	v_mul_f32_e32 v13, 0x3b808081, v13
	v_mul_f32_e32 v6, 0x3b808081, v6
	v_cvt_f32_ubyte0_e32 v15, v7
	v_cvt_f32_ubyte1_e32 v21, v7
	v_cvt_f32_ubyte2_e32 v192, v7
	v_cvt_f32_ubyte3_e32 v7, v7
	v_mul_f32_e32 v12, v104, v12
	v_mul_f32_e32 v13, v105, v13
	v_mul_f32_e32 v6, v107, v6
	v_mul_f32_e32 v15, 0x3b808081, v15
	v_mul_f32_e32 v21, 0x3b808081, v21
	v_mul_f32_e32 v7, 0x3b808081, v7
	v_mul_f32_e32 v12, 0x41800000, v12
	v_mul_f32_e32 v13, 0x41800000, v13
	v_mul_f32_e32 v6, 0x41800000, v6
	v_mul_f32_e32 v15, v100, v15
	v_mul_f32_e32 v21, v101, v21
	v_mul_f32_e32 v7, v103, v7
	v_med3_f32 v12, v12, s78, v198
	v_med3_f32 v13, v13, s78, v198
	v_med3_f32 v193, v6, s78, v198
	v_mov_b32_e32 v6, v3
	v_mul_f32_e32 v14, 0x3b808081, v14
	v_cvt_pk_fp8_f32 v6, v12, v13
	v_mul_f32_e32 v12, 0x41800000, v15
	v_mul_f32_e32 v13, 0x41800000, v21
	v_mul_f32_e32 v7, 0x41800000, v7
	v_mul_f32_e32 v14, v106, v14
	v_med3_f32 v12, v12, s78, v198
	v_med3_f32 v13, v13, s78, v198
	v_med3_f32 v15, v7, s78, v198
	v_mov_b32_e32 v7, v3
	v_mul_f32_e32 v192, 0x3b808081, v192
	v_mul_f32_e32 v14, 0x41800000, v14
	v_cvt_pk_fp8_f32 v7, v12, v13
	v_mul_f32_e32 v192, v102, v192
	v_med3_f32 v14, v14, s78, v198
	v_cvt_pk_fp8_f32 v6, v14, v193 op_sel:[0,0,1]
	v_mul_f32_e32 v14, 0x41800000, v192
	v_med3_f32 v14, v14, s78, v198
	v_cvt_pk_fp8_f32 v7, v14, v15 op_sel:[0,0,1]
	v_permlane16_swap_b32_e32 v4, v6
	v_cvt_f32_ubyte0_e32 v12, v8
	v_permlane16_swap_b32_e32 v5, v7
	global_store_dwordx4 v[26:27], v[4:7], off offset:128
	global_load_dwordx4 v[4:7], v[34:35], off offset:128
	v_cvt_f32_ubyte1_e32 v13, v8
	v_cvt_f32_ubyte2_e32 v14, v8
	v_cvt_f32_ubyte3_e32 v8, v8
	v_mul_f32_e32 v12, 0x3b808081, v12
	v_mul_f32_e32 v13, 0x3b808081, v13
	v_mul_f32_e32 v8, 0x3b808081, v8
	v_cvt_f32_ubyte0_e32 v15, v9
	v_cvt_f32_ubyte1_e32 v21, v9
	v_cvt_f32_ubyte2_e32 v26, v9
	v_cvt_f32_ubyte3_e32 v9, v9
	v_mul_f32_e32 v12, v96, v12
	v_mul_f32_e32 v13, v97, v13
	v_mul_f32_e32 v8, v99, v8
	v_mul_f32_e32 v15, 0x3b808081, v15
	v_mul_f32_e32 v21, 0x3b808081, v21
	v_mul_f32_e32 v9, 0x3b808081, v9
	v_mul_f32_e32 v12, 0x41800000, v12
	v_mul_f32_e32 v13, 0x41800000, v13
	v_mul_f32_e32 v8, 0x41800000, v8
	v_mul_f32_e32 v15, v92, v15
	v_mul_f32_e32 v21, v93, v21
	v_mul_f32_e32 v9, v95, v9
	v_med3_f32 v12, v12, s78, v198
	v_med3_f32 v13, v13, s78, v198
	v_med3_f32 v27, v8, s78, v198
	v_mov_b32_e32 v8, v3
	v_mul_f32_e32 v14, 0x3b808081, v14
	v_cvt_pk_fp8_f32 v8, v12, v13
	v_mul_f32_e32 v12, 0x41800000, v15
	v_mul_f32_e32 v13, 0x41800000, v21
	v_mul_f32_e32 v9, 0x41800000, v9
	v_mul_f32_e32 v14, v98, v14
	v_med3_f32 v12, v12, s78, v198
	v_med3_f32 v13, v13, s78, v198
	v_med3_f32 v15, v9, s78, v198
	v_mov_b32_e32 v9, v3
	v_mul_f32_e32 v26, 0x3b808081, v26
	v_mul_f32_e32 v14, 0x41800000, v14
	v_cvt_pk_fp8_f32 v9, v12, v13
	v_mul_f32_e32 v26, v94, v26
	v_med3_f32 v14, v14, s78, v198
	v_cvt_pk_fp8_f32 v8, v14, v27 op_sel:[0,0,1]
	v_mul_f32_e32 v14, 0x41800000, v26
	v_med3_f32 v14, v14, s78, v198
	v_cvt_pk_fp8_f32 v9, v14, v15 op_sel:[0,0,1]
	v_cvt_f32_ubyte0_e32 v12, v10
	v_cvt_f32_ubyte1_e32 v13, v10
	v_cvt_f32_ubyte2_e32 v14, v10
	v_cvt_f32_ubyte3_e32 v10, v10
	v_mul_f32_e32 v12, 0x3b808081, v12
	v_mul_f32_e32 v13, 0x3b808081, v13
	v_mul_f32_e32 v10, 0x3b808081, v10
	v_cvt_f32_ubyte0_e32 v15, v11
	v_cvt_f32_ubyte1_e32 v21, v11
	v_cvt_f32_ubyte2_e32 v26, v11
	v_cvt_f32_ubyte3_e32 v11, v11
	v_mul_f32_e32 v12, v88, v12
	v_mul_f32_e32 v13, v89, v13
	v_mul_f32_e32 v10, v91, v10
	v_mul_f32_e32 v15, 0x3b808081, v15
	v_mul_f32_e32 v21, 0x3b808081, v21
	v_mul_f32_e32 v11, 0x3b808081, v11
	v_mul_f32_e32 v12, 0x41800000, v12
	v_mul_f32_e32 v13, 0x41800000, v13
	v_mul_f32_e32 v10, 0x41800000, v10
	v_mul_f32_e32 v15, v84, v15
	v_mul_f32_e32 v21, v85, v21
	v_mul_f32_e32 v11, v87, v11
	v_med3_f32 v12, v12, s78, v198
	v_med3_f32 v13, v13, s78, v198
	v_med3_f32 v27, v10, s78, v198
	v_mov_b32_e32 v10, v3
	v_mul_f32_e32 v14, 0x3b808081, v14
	v_cvt_pk_fp8_f32 v10, v12, v13
	v_mul_f32_e32 v12, 0x41800000, v15
	v_mul_f32_e32 v13, 0x41800000, v21
	v_mul_f32_e32 v11, 0x41800000, v11
	v_mul_f32_e32 v14, v90, v14
	v_med3_f32 v12, v12, s78, v198
	v_med3_f32 v13, v13, s78, v198
	v_med3_f32 v15, v11, s78, v198
	v_mov_b32_e32 v11, v3
	v_mul_f32_e32 v26, 0x3b808081, v26
	v_mul_f32_e32 v14, 0x41800000, v14
	v_cvt_pk_fp8_f32 v11, v12, v13
	v_mul_f32_e32 v26, v86, v26
	v_med3_f32 v14, v14, s78, v198
	v_cvt_pk_fp8_f32 v10, v14, v27 op_sel:[0,0,1]
	v_mul_f32_e32 v14, 0x41800000, v26
	v_med3_f32 v14, v14, s78, v198
	v_ashrrev_i32_e32 v33, 31, v32
	v_cvt_pk_fp8_f32 v11, v14, v15 op_sel:[0,0,1]
	v_lshlrev_b64 v[12:13], 10, v[32:33]
	v_lshl_add_u64 v[12:13], s[10:11], 0, v[12:13]
	v_lshl_add_u64 v[12:13], v[12:13], 0, v[28:29]
	v_permlane16_swap_b32_e32 v8, v10
	v_permlane16_swap_b32_e32 v9, v11
	v_lshl_add_u64 v[12:13], v[12:13], 0, v[24:25]
	global_store_dwordx4 v[12:13], v[8:11], off
	global_load_dwordx4 v[8:11], v[164:165], off offset:128
	s_waitcnt vmcnt(4)
	v_mov_b32_e32 v14, v18
	s_nop 1
	v_permlane16_swap_b32_e32 v16, v14
	v_mov_b32_e32 v15, v19
	s_nop 1
	v_permlane16_swap_b32_e32 v17, v15
	v_cvt_f32_ubyte0_e32 v18, v16
	v_cvt_f32_ubyte1_e32 v19, v16
	v_cvt_f32_ubyte2_e32 v21, v16
	v_cvt_f32_ubyte3_e32 v16, v16
	v_mul_f32_e32 v18, 0x3b808081, v18
	v_mul_f32_e32 v19, 0x3b808081, v19
	v_mul_f32_e32 v16, 0x3b808081, v16
	v_cvt_f32_ubyte0_e32 v26, v17
	v_cvt_f32_ubyte1_e32 v27, v17
	v_cvt_f32_ubyte2_e32 v33, v17
	v_cvt_f32_ubyte3_e32 v17, v17
	v_mul_f32_e32 v18, v80, v18
	v_mul_f32_e32 v19, v81, v19
	v_mul_f32_e32 v16, v83, v16
	v_mul_f32_e32 v26, 0x3b808081, v26
	v_mul_f32_e32 v27, 0x3b808081, v27
	v_mul_f32_e32 v17, 0x3b808081, v17
	v_mul_f32_e32 v18, 0x41800000, v18
	v_mul_f32_e32 v19, 0x41800000, v19
	v_mul_f32_e32 v16, 0x41800000, v16
	v_mul_f32_e32 v26, v76, v26
	v_mul_f32_e32 v27, v77, v27
	v_mul_f32_e32 v17, v79, v17
	v_med3_f32 v18, v18, s78, v198
	v_med3_f32 v19, v19, s78, v198
	v_med3_f32 v34, v16, s78, v198
	v_mov_b32_e32 v16, v3
	v_mul_f32_e32 v21, 0x3b808081, v21
	v_cvt_pk_fp8_f32 v16, v18, v19
	v_mul_f32_e32 v18, 0x41800000, v26
	v_mul_f32_e32 v19, 0x41800000, v27
	v_mul_f32_e32 v17, 0x41800000, v17
	v_mul_f32_e32 v21, v82, v21
	v_med3_f32 v18, v18, s78, v198
	v_med3_f32 v19, v19, s78, v198
	v_med3_f32 v26, v17, s78, v198
	v_mov_b32_e32 v17, v3
	v_mul_f32_e32 v33, 0x3b808081, v33
	v_mul_f32_e32 v21, 0x41800000, v21
	v_cvt_pk_fp8_f32 v17, v18, v19
	v_mul_f32_e32 v33, v78, v33
	v_med3_f32 v21, v21, s78, v198
	v_cvt_pk_fp8_f32 v16, v21, v34 op_sel:[0,0,1]
	v_mul_f32_e32 v21, 0x41800000, v33
	v_cvt_f32_ubyte0_e32 v18, v14
	v_med3_f32 v21, v21, s78, v198
	v_cvt_f32_ubyte1_e32 v19, v14
	v_mul_f32_e32 v18, 0x3b808081, v18
	v_cvt_pk_fp8_f32 v17, v21, v26 op_sel:[0,0,1]
	v_cvt_f32_ubyte2_e32 v21, v14
	v_mul_f32_e32 v19, 0x3b808081, v19
	v_mul_f32_e32 v18, v72, v18
	v_mul_f32_e32 v21, 0x3b808081, v21
	v_mul_f32_e32 v19, v73, v19
	v_mul_f32_e32 v18, 0x41800000, v18
	v_mul_f32_e32 v21, v74, v21
	v_med3_f32 v34, v18, s78, v198
	v_mul_f32_e32 v18, 0x41800000, v19
	v_med3_f32 v19, v18, s78, v198
	v_mul_f32_e32 v18, 0x41800000, v21
	v_cvt_f32_ubyte3_e32 v14, v14
	v_med3_f32 v21, v18, s78, v198
	v_mov_b32_e32 v18, v3
	v_cvt_f32_ubyte1_e32 v27, v15
	v_mul_f32_e32 v14, 0x3b808081, v14
	v_cvt_pk_fp8_f32 v18, v34, v19
	v_cvt_f32_ubyte0_e32 v26, v15
	v_cvt_f32_ubyte2_e32 v33, v15
	v_mul_f32_e32 v27, 0x3b808081, v27
	v_mul_f32_e32 v14, v75, v14
	v_mul_f32_e32 v26, 0x3b808081, v26
	v_mul_f32_e32 v33, 0x3b808081, v33
	v_mul_f32_e32 v27, v69, v27
	v_mul_f32_e32 v14, 0x41800000, v14
	v_mul_f32_e32 v26, v68, v26
	v_mul_f32_e32 v33, v70, v33
	v_med3_f32 v14, v14, s78, v198
	v_mul_f32_e32 v19, 0x41800000, v27
	v_cvt_pk_fp8_f32 v18, v21, v14 op_sel:[0,0,1]
	v_mul_f32_e32 v14, 0x41800000, v26
	v_med3_f32 v21, v19, s78, v198
	v_mul_f32_e32 v19, 0x41800000, v33
	v_cvt_f32_ubyte3_e32 v15, v15
	v_med3_f32 v14, v14, s78, v198
	v_med3_f32 v26, v19, s78, v198
	v_mov_b32_e32 v19, v3
	v_mul_f32_e32 v15, 0x3b808081, v15
	v_cvt_pk_fp8_f32 v19, v14, v21
	v_mul_f32_e32 v15, v71, v15
	v_mul_f32_e32 v15, 0x41800000, v15
	v_med3_f32 v15, v15, s78, v198
	v_ashrrev_i32_e32 v31, 31, v30
	v_cvt_pk_fp8_f32 v19, v26, v15 op_sel:[0,0,1]
	v_lshlrev_b64 v[14:15], 10, v[30:31]
	v_lshl_add_u64 v[14:15], s[10:11], 0, v[14:15]
	v_lshl_add_u64 v[14:15], v[14:15], 0, v[28:29]
	v_permlane16_swap_b32_e32 v16, v18
	v_permlane16_swap_b32_e32 v17, v19
	v_lshl_add_u64 v[14:15], v[14:15], 0, v[24:25]
	global_store_dwordx4 v[14:15], v[16:19], off
	s_waitcnt vmcnt(3)
	v_permlane16_swap_b32_e32 v4, v6
	v_permlane16_swap_b32_e32 v5, v7
	v_cvt_f32_ubyte0_e32 v16, v4
	v_cvt_f32_ubyte1_e32 v17, v4
	v_cvt_f32_ubyte2_e32 v18, v4
	v_cvt_f32_ubyte3_e32 v4, v4
	v_mul_f32_e32 v16, 0x3b808081, v16
	v_mul_f32_e32 v17, 0x3b808081, v17
	v_mul_f32_e32 v4, 0x3b808081, v4
	v_cvt_f32_ubyte0_e32 v19, v5
	v_cvt_f32_ubyte1_e32 v21, v5
	v_cvt_f32_ubyte2_e32 v24, v5
	v_cvt_f32_ubyte3_e32 v5, v5
	v_mul_f32_e32 v16, v64, v16
	v_mul_f32_e32 v17, v65, v17
	v_mul_f32_e32 v4, v67, v4
	v_mul_f32_e32 v19, 0x3b808081, v19
	v_mul_f32_e32 v21, 0x3b808081, v21
	v_mul_f32_e32 v5, 0x3b808081, v5
	v_mul_f32_e32 v16, 0x41800000, v16
	v_mul_f32_e32 v17, 0x41800000, v17
	v_mul_f32_e32 v4, 0x41800000, v4
	v_mul_f32_e32 v19, v60, v19
	v_mul_f32_e32 v21, v61, v21
	v_mul_f32_e32 v5, v63, v5
	v_med3_f32 v16, v16, s78, v198
	v_med3_f32 v17, v17, s78, v198
	v_med3_f32 v25, v4, s78, v198
	v_mov_b32_e32 v4, v3
	v_mul_f32_e32 v18, 0x3b808081, v18
	v_cvt_pk_fp8_f32 v4, v16, v17
	v_mul_f32_e32 v16, 0x41800000, v19
	v_mul_f32_e32 v17, 0x41800000, v21
	v_mul_f32_e32 v5, 0x41800000, v5
	v_mul_f32_e32 v18, v66, v18
	v_med3_f32 v16, v16, s78, v198
	v_med3_f32 v17, v17, s78, v198
	v_med3_f32 v19, v5, s78, v198
	v_mov_b32_e32 v5, v3
	v_mul_f32_e32 v24, 0x3b808081, v24
	v_mul_f32_e32 v18, 0x41800000, v18
	v_cvt_pk_fp8_f32 v5, v16, v17
	v_mul_f32_e32 v24, v62, v24
	v_med3_f32 v18, v18, s78, v198
	v_cvt_pk_fp8_f32 v4, v18, v25 op_sel:[0,0,1]
	v_mul_f32_e32 v18, 0x41800000, v24
	v_med3_f32 v18, v18, s78, v198
	v_cvt_pk_fp8_f32 v5, v18, v19 op_sel:[0,0,1]
	v_cvt_f32_ubyte0_e32 v16, v6
	v_cvt_f32_ubyte1_e32 v17, v6
	v_cvt_f32_ubyte2_e32 v18, v6
	v_cvt_f32_ubyte3_e32 v6, v6
	v_mul_f32_e32 v16, 0x3b808081, v16
	v_mul_f32_e32 v17, 0x3b808081, v17
	v_mul_f32_e32 v6, 0x3b808081, v6
	v_cvt_f32_ubyte0_e32 v19, v7
	v_cvt_f32_ubyte1_e32 v21, v7
	v_cvt_f32_ubyte2_e32 v24, v7
	v_cvt_f32_ubyte3_e32 v7, v7
	v_mul_f32_e32 v16, v56, v16
	v_mul_f32_e32 v17, v57, v17
	v_mul_f32_e32 v6, v59, v6
	v_mul_f32_e32 v19, 0x3b808081, v19
	v_mul_f32_e32 v21, 0x3b808081, v21
	v_mul_f32_e32 v7, 0x3b808081, v7
	v_mul_f32_e32 v16, 0x41800000, v16
	v_mul_f32_e32 v17, 0x41800000, v17
	v_mul_f32_e32 v6, 0x41800000, v6
	v_mul_f32_e32 v19, v52, v19
	v_mul_f32_e32 v21, v53, v21
	v_mul_f32_e32 v7, v55, v7
	v_med3_f32 v16, v16, s78, v198
	v_med3_f32 v17, v17, s78, v198
	v_med3_f32 v25, v6, s78, v198
	v_mov_b32_e32 v6, v3
	v_mul_f32_e32 v18, 0x3b808081, v18
	v_cvt_pk_fp8_f32 v6, v16, v17
	v_mul_f32_e32 v16, 0x41800000, v19
	v_mul_f32_e32 v17, 0x41800000, v21
	v_mul_f32_e32 v7, 0x41800000, v7
	v_mul_f32_e32 v18, v58, v18
	v_med3_f32 v16, v16, s78, v198
	v_med3_f32 v17, v17, s78, v198
	v_med3_f32 v19, v7, s78, v198
	v_mov_b32_e32 v7, v3
	v_mul_f32_e32 v24, 0x3b808081, v24
	v_mul_f32_e32 v18, 0x41800000, v18
	v_cvt_pk_fp8_f32 v7, v16, v17
	v_mul_f32_e32 v24, v54, v24
	v_med3_f32 v18, v18, s78, v198
	v_cvt_pk_fp8_f32 v6, v18, v25 op_sel:[0,0,1]
	v_mul_f32_e32 v18, 0x41800000, v24
	v_med3_f32 v18, v18, s78, v198
	v_cvt_pk_fp8_f32 v7, v18, v19 op_sel:[0,0,1]
	v_permlane16_swap_b32_e32 v4, v6
	s_nop 0
	v_permlane16_swap_b32_e32 v5, v7
	global_store_dwordx4 v[12:13], v[4:7], off offset:128
	s_waitcnt vmcnt(2)
	s_nop 0
	v_mov_b32_e32 v6, v10
	s_nop 1
	v_permlane16_swap_b32_e32 v8, v6
	v_cvt_f32_ubyte0_e32 v4, v8
	v_cvt_f32_ubyte1_e32 v5, v8
	v_mul_f32_e32 v4, 0x3b808081, v4
	v_mov_b32_e32 v7, v11
	v_cvt_f32_ubyte2_e32 v10, v8
	v_mul_f32_e32 v5, 0x3b808081, v5
	v_mul_f32_e32 v4, v48, v4
	v_permlane16_swap_b32_e32 v9, v7
	v_cvt_f32_ubyte3_e32 v8, v8
	v_mul_f32_e32 v10, 0x3b808081, v10
	v_mul_f32_e32 v5, v49, v5
	v_mul_f32_e32 v4, 0x41800000, v4
	v_mul_f32_e32 v8, 0x3b808081, v8
	v_mul_f32_e32 v10, v50, v10
	v_med3_f32 v16, v4, s78, v198
	v_mul_f32_e32 v4, 0x41800000, v5
	v_mul_f32_e32 v8, v51, v8
	v_med3_f32 v5, v4, s78, v198
	v_mul_f32_e32 v4, 0x41800000, v10
	v_med3_f32 v10, v4, s78, v198
	v_mul_f32_e32 v4, 0x41800000, v8
	v_med3_f32 v8, v4, s78, v198
	v_mov_b32_e32 v4, v3
	v_cvt_f32_ubyte0_e32 v11, v9
	v_cvt_pk_fp8_f32 v4, v16, v5
	v_cvt_f32_ubyte1_e32 v12, v9
	v_mul_f32_e32 v11, 0x3b808081, v11
	v_cvt_f32_ubyte2_e32 v13, v9
	v_mul_f32_e32 v12, 0x3b808081, v12
	v_mul_f32_e32 v11, v44, v11
	v_cvt_f32_ubyte3_e32 v9, v9
	v_mul_f32_e32 v13, 0x3b808081, v13
	v_mul_f32_e32 v12, v45, v12
	v_mul_f32_e32 v5, 0x41800000, v11
	v_mul_f32_e32 v9, 0x3b808081, v9
	v_mul_f32_e32 v13, v46, v13
	v_cvt_pk_fp8_f32 v4, v10, v8 op_sel:[0,0,1]
	v_med3_f32 v8, v5, s78, v198
	v_mul_f32_e32 v5, 0x41800000, v12
	v_mul_f32_e32 v9, v47, v9
	v_med3_f32 v10, v5, s78, v198
	v_mul_f32_e32 v5, 0x41800000, v13
	v_med3_f32 v11, v5, s78, v198
	v_mul_f32_e32 v5, 0x41800000, v9
	v_med3_f32 v9, v5, s78, v198
	v_mov_b32_e32 v5, v3
	v_cvt_pk_fp8_f32 v5, v8, v10
	v_cvt_f32_ubyte0_e32 v8, v6
	v_cvt_f32_ubyte2_e32 v10, v6
	v_cvt_pk_fp8_f32 v5, v11, v9 op_sel:[0,0,1]
	v_cvt_f32_ubyte1_e32 v9, v6
	v_cvt_f32_ubyte3_e32 v6, v6
	v_mul_f32_e32 v8, 0x3b808081, v8
	v_mul_f32_e32 v9, 0x3b808081, v9
	v_mul_f32_e32 v6, 0x3b808081, v6
	v_cvt_f32_ubyte0_e32 v11, v7
	v_cvt_f32_ubyte1_e32 v12, v7
	v_cvt_f32_ubyte2_e32 v13, v7
	v_cvt_f32_ubyte3_e32 v7, v7
	v_mul_f32_e32 v8, v40, v8
	v_mul_f32_e32 v9, v41, v9
	v_mul_f32_e32 v6, v43, v6
	v_mul_f32_e32 v11, 0x3b808081, v11
	v_mul_f32_e32 v12, 0x3b808081, v12
	v_mul_f32_e32 v7, 0x3b808081, v7
	v_mul_f32_e32 v8, 0x41800000, v8
	v_mul_f32_e32 v9, 0x41800000, v9
	v_mul_f32_e32 v6, 0x41800000, v6
	v_mul_f32_e32 v11, v36, v11
	v_mul_f32_e32 v12, v37, v12
	v_mul_f32_e32 v7, v39, v7
	v_med3_f32 v8, v8, s78, v198
	v_med3_f32 v9, v9, s78, v198
	v_med3_f32 v16, v6, s78, v198
	v_mov_b32_e32 v6, v3
	v_mul_f32_e32 v10, 0x3b808081, v10
	v_cvt_pk_fp8_f32 v6, v8, v9
	v_mul_f32_e32 v8, 0x41800000, v11
	v_mul_f32_e32 v9, 0x41800000, v12
	v_mul_f32_e32 v7, 0x41800000, v7
	v_mul_f32_e32 v10, v42, v10
	v_med3_f32 v8, v8, s78, v198
	v_med3_f32 v9, v9, s78, v198
	v_med3_f32 v11, v7, s78, v198
	v_mov_b32_e32 v7, v3
	v_mul_f32_e32 v13, 0x3b808081, v13
	v_mul_f32_e32 v10, 0x41800000, v10
	v_cvt_pk_fp8_f32 v7, v8, v9
	v_mul_f32_e32 v13, v38, v13
	v_med3_f32 v10, v10, s78, v198
	v_cvt_pk_fp8_f32 v6, v10, v16 op_sel:[0,0,1]
	v_mul_f32_e32 v10, 0x41800000, v13
	v_med3_f32 v10, v10, s78, v198
	v_cvt_pk_fp8_f32 v7, v10, v11 op_sel:[0,0,1]
	v_permlane16_swap_b32_e32 v4, v6
	s_nop 0
	v_permlane16_swap_b32_e32 v5, v7
	global_store_dwordx4 v[14:15], v[4:7], off offset:128
	s_cbranch_execz .LBB0_916

.LBB0_1017:
	s_or_b64 exec, exec, s[2:3]
	v_mov_b32_e32 v2, v0
	s_nop 11
	s_mov_b64 s[2:3], -1
	v_ashrrev_i32_e32 v4, 2, v2
	v_and_b32_e32 v4, 0xffffffc0, v4
	v_lshl_add_u32 v4, s23, 8, v4
	v_and_or_b32 v28, v2, 15, v4
	v_lshrrev_b32_e32 v2, 1, v2
	v_and_b32_e32 v2, 0x78, v2
	v_or_b32_e32 v32, s24, v2
	v_readlane_b32 s24, v254, 13
	v_readlane_b32 s25, v254, 14
	v_or_b32_e32 v182, 16, v28
	v_or_b32_e32 v180, 32, v28
	v_or_b32_e32 v30, 48, v28
	s_and_b64 vcc, exec, s[24:25]
	v_ashrrev_i32_e32 v33, 31, v32
	v_ashrrev_i32_e32 v29, 31, v28
	v_ashrrev_i32_e32 v183, 31, v182
	v_ashrrev_i32_e32 v181, 31, v180
	v_ashrrev_i32_e32 v31, 31, v30
	s_cbranch_vccz .LBB0_1020
	v_lshl_add_u64 v[10:11], v[32:33], 1, s[12:13]
	v_lshlrev_b64 v[4:5], 11, v[28:29]
	v_lshl_add_u64 v[8:9], v[10:11], 0, v[4:5]
	global_load_dwordx4 v[4:7], v[8:9], off
	v_lshlrev_b64 v[12:13], 11, v[182:183]
	v_lshl_add_u64 v[18:19], v[10:11], 0, v[12:13]
	v_lshlrev_b64 v[16:17], 11, v[180:181]
	v_lshlrev_b64 v[24:25], 11, v[30:31]
	global_load_dwordx4 v[12:15], v[18:19], off
	v_lshl_add_u64 v[16:17], v[10:11], 0, v[16:17]
	v_lshl_add_u64 v[10:11], v[10:11], 0, v[24:25]
	global_load_dwordx4 v[20:23], v[16:17], off
	global_load_dwordx4 v[184:187], v[10:11], off
	global_load_dwordx4 v[190:193], v[8:9], off offset:256
	global_load_dwordx4 v[230:233], v[18:19], off offset:256
	global_load_dwordx4 v[234:237], v[16:17], off offset:256
	global_load_dwordx4 v[238:241], v[10:11], off offset:256
	s_mov_b64 s[2:3], 0x40000
	v_lshl_add_u64 v[24:25], v[8:9], 0, s[2:3]
	s_mov_b32 s2, 0x40000
	s_waitcnt vmcnt(0)
	v_lshlrev_b32_e32 v26, 16, v4
	v_and_b32_e32 v27, 0xffff0000, v4
	v_lshlrev_b32_e32 v4, 16, v5
	v_and_b32_e32 v5, 0xffff0000, v5
	v_lshlrev_b32_e32 v34, 16, v6
	v_and_b32_e32 v35, 0xffff0000, v6
	v_lshlrev_b32_e32 v6, 16, v7
	v_and_b32_e32 v7, 0xffff0000, v7
	v_pk_fma_f32 v[250:251], v[38:39], v[178:179], v[4:5]
	v_pk_fma_f32 v[4:5], v[36:37], v[176:177], v[26:27]
	v_pk_fma_f32 v[26:27], v[42:43], v[174:175], v[6:7]
	v_pk_fma_f32 v[6:7], v[40:41], v[172:173], v[34:35]
	v_lshlrev_b32_e32 v188, 16, v12
	v_and_b32_e32 v189, 0xffff0000, v12
	v_lshlrev_b32_e32 v12, 16, v13
	v_and_b32_e32 v13, 0xffff0000, v13
	v_lshlrev_b32_e32 v194, 16, v14
	v_and_b32_e32 v195, 0xffff0000, v14
	v_cvt_pk_bf16_f32 v4, v4, v5
	v_cvt_pk_bf16_f32 v5, v250, v251
	v_cvt_pk_bf16_f32 v6, v6, v7
	v_lshlrev_b32_e32 v14, 16, v15
	v_and_b32_e32 v15, 0xffff0000, v15
	v_lshlrev_b32_e32 v242, 16, v20
	v_and_b32_e32 v243, 0xffff0000, v20
	v_lshlrev_b32_e32 v20, 16, v21
	v_and_b32_e32 v21, 0xffff0000, v21
	v_lshlrev_b32_e32 v244, 16, v22
	v_and_b32_e32 v245, 0xffff0000, v22
	v_lshlrev_b32_e32 v246, 16, v184
	v_and_b32_e32 v247, 0xffff0000, v184
	v_lshlrev_b32_e32 v248, 16, v186
	v_and_b32_e32 v249, 0xffff0000, v186
	v_pk_fma_f32 v[12:13], v[38:39], v[170:171], v[12:13]
	v_pk_fma_f32 v[34:35], v[36:37], v[168:169], v[188:189]
	v_pk_fma_f32 v[188:189], v[40:41], v[164:165], v[194:195]
	v_cvt_pk_bf16_f32 v7, v26, v27
	global_store_dwordx4 v[8:9], v[4:7], off
	v_lshlrev_b32_e32 v22, 16, v23
	v_and_b32_e32 v23, 0xffff0000, v23
	v_cvt_pk_bf16_f32 v4, v34, v35
	v_cvt_pk_bf16_f32 v5, v12, v13
	v_cvt_pk_bf16_f32 v6, v188, v189
	v_lshlrev_b32_e32 v184, 16, v185
	v_and_b32_e32 v185, 0xffff0000, v185
	v_pk_fma_f32 v[14:15], v[42:43], v[166:167], v[14:15]
	v_pk_fma_f32 v[20:21], v[38:39], v[162:163], v[20:21]
	v_pk_fma_f32 v[194:195], v[36:37], v[160:161], v[242:243]
	v_pk_fma_f32 v[242:243], v[40:41], v[156:157], v[244:245]
	v_pk_fma_f32 v[244:245], v[36:37], v[152:153], v[246:247]
	v_pk_fma_f32 v[246:247], v[40:41], v[148:149], v[248:249]
	v_cvt_pk_bf16_f32 v7, v14, v15
	global_store_dwordx4 v[18:19], v[4:7], off
	v_pk_fma_f32 v[22:23], v[42:43], v[158:159], v[22:23]
	v_pk_fma_f32 v[184:185], v[38:39], v[154:155], v[184:185]
	v_cvt_pk_bf16_f32 v4, v194, v195
	v_cvt_pk_bf16_f32 v5, v20, v21
	v_cvt_pk_bf16_f32 v6, v242, v243
	v_cvt_pk_bf16_f32 v7, v22, v23
	global_store_dwordx4 v[16:17], v[4:7], off
	v_lshlrev_b32_e32 v186, 16, v187
	v_and_b32_e32 v187, 0xffff0000, v187
	v_cvt_pk_bf16_f32 v4, v244, v245
	v_cvt_pk_bf16_f32 v5, v184, v185
	v_cvt_pk_bf16_f32 v6, v246, v247
	v_add_co_u32_e32 v246, vcc, s2, v8
	s_mov_b32 s2, 0x48000
	s_nop 0
	v_addc_co_u32_e32 v247, vcc, 0, v9, vcc
	v_pk_fma_f32 v[186:187], v[42:43], v[150:151], v[186:187]
	v_add_co_u32_e32 v188, vcc, s2, v8
	v_cvt_pk_bf16_f32 v7, v186, v187
	global_store_dwordx4 v[10:11], v[4:7], off
	s_nop 0
	v_addc_co_u32_e32 v189, vcc, 0, v9, vcc
	s_mov_b32 s2, 0x50000
	global_load_dwordx4 v[242:245], v[246:247], off
	global_load_dwordx4 v[20:23], v[188:189], off
	v_add_co_u32_e32 v184, vcc, s2, v8
	s_mov_b32 s2, 0x58000
	s_nop 0
	v_addc_co_u32_e32 v185, vcc, 0, v9, vcc
	v_lshlrev_b32_e32 v34, 16, v190
	v_and_b32_e32 v35, 0xffff0000, v190
	v_lshlrev_b32_e32 v186, 16, v191
	v_and_b32_e32 v187, 0xffff0000, v191
	v_lshlrev_b32_e32 v190, 16, v192
	v_and_b32_e32 v191, 0xffff0000, v192
	v_lshlrev_b32_e32 v192, 16, v193
	v_and_b32_e32 v193, 0xffff0000, v193
	v_add_co_u32_e32 v26, vcc, s2, v8
	v_pk_fma_f32 v[194:195], v[50:51], v[142:143], v[192:193]
	v_pk_fma_f32 v[192:193], v[48:49], v[140:141], v[190:191]
	v_addc_co_u32_e32 v27, vcc, 0, v9, vcc
	global_load_dwordx4 v[12:15], v[184:185], off
	global_load_dwordx4 v[4:7], v[26:27], off
	v_pk_fma_f32 v[186:187], v[46:47], v[146:147], v[186:187]
	v_pk_fma_f32 v[34:35], v[44:45], v[144:145], v[34:35]
	s_mov_b64 s[2:3], 0x48000
	v_cvt_pk_bf16_f32 v190, v34, v35
	v_cvt_pk_bf16_f32 v191, v186, v187
	v_cvt_pk_bf16_f32 v192, v192, v193
	v_cvt_pk_bf16_f32 v193, v194, v195
	global_store_dwordx4 v[8:9], v[190:193], off offset:256
	v_lshlrev_b32_e32 v34, 16, v230
	v_and_b32_e32 v35, 0xffff0000, v230
	v_lshlrev_b32_e32 v190, 16, v232
	v_and_b32_e32 v191, 0xffff0000, v232
	v_lshlrev_b32_e32 v192, 16, v233
	v_and_b32_e32 v193, 0xffff0000, v233
	v_lshlrev_b32_e32 v186, 16, v231
	v_and_b32_e32 v187, 0xffff0000, v231
	v_pk_fma_f32 v[194:195], v[50:51], v[134:135], v[192:193]
	v_pk_fma_f32 v[192:193], v[48:49], v[132:133], v[190:191]
	v_pk_fma_f32 v[186:187], v[46:47], v[138:139], v[186:187]
	v_pk_fma_f32 v[34:35], v[44:45], v[136:137], v[34:35]
	s_nop 0
	v_cvt_pk_bf16_f32 v190, v34, v35
	v_cvt_pk_bf16_f32 v191, v186, v187
	v_cvt_pk_bf16_f32 v192, v192, v193
	v_cvt_pk_bf16_f32 v193, v194, v195
	global_store_dwordx4 v[18:19], v[190:193], off offset:256
	v_lshlrev_b32_e32 v18, 16, v234
	v_and_b32_e32 v19, 0xffff0000, v234
	v_lshlrev_b32_e32 v34, 16, v235
	v_and_b32_e32 v35, 0xffff0000, v235
	v_pk_fma_f32 v[18:19], v[44:45], v[128:129], v[18:19]
	v_lshlrev_b32_e32 v186, 16, v236
	v_and_b32_e32 v187, 0xffff0000, v236
	v_lshlrev_b32_e32 v190, 16, v237
	v_and_b32_e32 v191, 0xffff0000, v237
	v_pk_fma_f32 v[34:35], v[46:47], v[130:131], v[34:35]
	v_pk_fma_f32 v[194:195], v[50:51], v[126:127], v[190:191]
	v_pk_fma_f32 v[186:187], v[48:49], v[124:125], v[186:187]
	v_cvt_pk_bf16_f32 v190, v18, v19
	v_cvt_pk_bf16_f32 v191, v34, v35
	v_lshlrev_b32_e32 v18, 16, v239
	v_cvt_pk_bf16_f32 v192, v186, v187
	v_cvt_pk_bf16_f32 v193, v194, v195
	global_store_dwordx4 v[16:17], v[190:193], off offset:256
	v_lshlrev_b32_e32 v16, 16, v238
	v_and_b32_e32 v17, 0xffff0000, v238
	v_and_b32_e32 v19, 0xffff0000, v239
	v_pk_fma_f32 v[18:19], v[46:47], v[122:123], v[18:19]
	v_pk_fma_f32 v[16:17], v[44:45], v[120:121], v[16:17]
	v_lshlrev_b32_e32 v34, 16, v240
	v_and_b32_e32 v35, 0xffff0000, v240
	v_lshlrev_b32_e32 v186, 16, v241
	v_and_b32_e32 v187, 0xffff0000, v241
	v_pk_fma_f32 v[186:187], v[50:51], v[118:119], v[186:187]
	v_pk_fma_f32 v[34:35], v[48:49], v[116:117], v[34:35]
	v_cvt_pk_bf16_f32 v16, v16, v17
	v_cvt_pk_bf16_f32 v17, v18, v19
	v_lshl_add_u64 v[190:191], v[8:9], 0, s[2:3]
	v_cvt_pk_bf16_f32 v18, v34, v35
	v_cvt_pk_bf16_f32 v19, v186, v187
	global_store_dwordx4 v[10:11], v[16:19], off offset:256
	global_load_dwordx4 v[192:195], v[24:25], off offset:256
	s_mov_b64 s[2:3], 0x50000
	v_lshl_add_u64 v[186:187], v[8:9], 0, s[2:3]
	s_mov_b64 s[2:3], 0x58000
	v_lshl_add_u64 v[34:35], v[8:9], 0, s[2:3]
	global_load_dwordx4 v[230:233], v[190:191], off offset:256
	global_load_dwordx4 v[16:19], v[186:187], off offset:256
	global_load_dwordx4 v[8:11], v[34:35], off offset:256
	s_waitcnt vmcnt(11)
	v_lshlrev_b32_e32 v234, 16, v242
	v_and_b32_e32 v235, 0xffff0000, v242
	v_lshlrev_b32_e32 v236, 16, v243
	v_and_b32_e32 v237, 0xffff0000, v243
	v_pk_fma_f32 v[234:235], v[36:37], v[112:113], v[234:235]
	v_pk_fma_f32 v[236:237], v[38:39], v[114:115], v[236:237]
	v_lshlrev_b32_e32 v238, 16, v244
	v_and_b32_e32 v239, 0xffff0000, v244
	v_lshlrev_b32_e32 v240, 16, v245
	v_and_b32_e32 v241, 0xffff0000, v245
	v_cvt_pk_bf16_f32 v234, v234, v235
	v_cvt_pk_bf16_f32 v235, v236, v237
	v_pk_fma_f32 v[240:241], v[42:43], v[110:111], v[240:241]
	v_pk_fma_f32 v[238:239], v[40:41], v[108:109], v[238:239]
	s_nop 0
	v_cvt_pk_bf16_f32 v236, v238, v239
	v_cvt_pk_bf16_f32 v237, v240, v241
	global_store_dwordx4 v[246:247], v[234:237], off
	s_waitcnt vmcnt(11)
	s_nop 0
	v_lshlrev_b32_e32 v234, 16, v20
	v_and_b32_e32 v235, 0xffff0000, v20
	v_lshlrev_b32_e32 v20, 16, v21
	v_and_b32_e32 v21, 0xffff0000, v21
	v_pk_fma_f32 v[236:237], v[38:39], v[106:107], v[20:21]
	v_pk_fma_f32 v[20:21], v[36:37], v[104:105], v[234:235]
	v_lshlrev_b32_e32 v234, 16, v22
	v_and_b32_e32 v235, 0xffff0000, v22
	v_lshlrev_b32_e32 v22, 16, v23
	v_and_b32_e32 v23, 0xffff0000, v23
	v_pk_fma_f32 v[238:239], v[42:43], v[102:103], v[22:23]
	v_pk_fma_f32 v[22:23], v[40:41], v[100:101], v[234:235]
	v_cvt_pk_bf16_f32 v20, v20, v21
	v_cvt_pk_bf16_f32 v21, v236, v237
	s_nop 0
	v_cvt_pk_bf16_f32 v22, v22, v23
	v_cvt_pk_bf16_f32 v23, v238, v239
	global_store_dwordx4 v[188:189], v[20:23], off
	s_waitcnt vmcnt(11)
	s_nop 0
	v_lshlrev_b32_e32 v20, 16, v12
	v_and_b32_e32 v21, 0xffff0000, v12
	v_lshlrev_b32_e32 v12, 16, v13
	v_and_b32_e32 v13, 0xffff0000, v13
	v_pk_fma_f32 v[22:23], v[38:39], v[98:99], v[12:13]
	v_pk_fma_f32 v[12:13], v[36:37], v[96:97], v[20:21]
	v_lshlrev_b32_e32 v20, 16, v14
	v_and_b32_e32 v21, 0xffff0000, v14
	v_lshlrev_b32_e32 v14, 16, v15
	v_and_b32_e32 v15, 0xffff0000, v15
	v_pk_fma_f32 v[188:189], v[42:43], v[94:95], v[14:15]
	v_pk_fma_f32 v[14:15], v[40:41], v[92:93], v[20:21]
	v_cvt_pk_bf16_f32 v12, v12, v13
	v_cvt_pk_bf16_f32 v13, v22, v23
	s_nop 0
	v_cvt_pk_bf16_f32 v14, v14, v15
	v_cvt_pk_bf16_f32 v15, v188, v189
	global_store_dwordx4 v[184:185], v[12:15], off
	s_waitcnt vmcnt(11)
	s_nop 0
	v_lshlrev_b32_e32 v12, 16, v4
	v_and_b32_e32 v13, 0xffff0000, v4
	v_lshlrev_b32_e32 v4, 16, v5
	v_and_b32_e32 v5, 0xffff0000, v5
	v_pk_fma_f32 v[14:15], v[38:39], v[90:91], v[4:5]
	v_pk_fma_f32 v[4:5], v[36:37], v[88:89], v[12:13]
	v_lshlrev_b32_e32 v12, 16, v6
	v_and_b32_e32 v13, 0xffff0000, v6
	v_lshlrev_b32_e32 v6, 16, v7
	v_and_b32_e32 v7, 0xffff0000, v7
	v_pk_fma_f32 v[20:21], v[42:43], v[86:87], v[6:7]
	v_pk_fma_f32 v[6:7], v[40:41], v[84:85], v[12:13]
	v_cvt_pk_bf16_f32 v4, v4, v5
	v_cvt_pk_bf16_f32 v5, v14, v15
	s_waitcnt vmcnt(6)
	v_lshlrev_b32_e32 v12, 16, v194
	v_cvt_pk_bf16_f32 v6, v6, v7
	v_cvt_pk_bf16_f32 v7, v20, v21
	global_store_dwordx4 v[26:27], v[4:7], off
	v_and_b32_e32 v13, 0xffff0000, v194
	v_lshlrev_b32_e32 v14, 16, v195
	v_lshlrev_b32_e32 v4, 16, v192
	v_and_b32_e32 v5, 0xffff0000, v192
	v_lshlrev_b32_e32 v6, 16, v193
	v_and_b32_e32 v7, 0xffff0000, v193
	v_pk_fma_f32 v[6:7], v[46:47], v[82:83], v[6:7]
	v_pk_fma_f32 v[4:5], v[44:45], v[80:81], v[4:5]
	v_and_b32_e32 v15, 0xffff0000, v195
	v_pk_fma_f32 v[14:15], v[50:51], v[78:79], v[14:15]
	v_pk_fma_f32 v[12:13], v[48:49], v[76:77], v[12:13]
	v_cvt_pk_bf16_f32 v4, v4, v5
	v_cvt_pk_bf16_f32 v5, v6, v7
	s_nop 0
	v_cvt_pk_bf16_f32 v6, v12, v13
	v_cvt_pk_bf16_f32 v7, v14, v15
	global_store_dwordx4 v[24:25], v[4:7], off offset:256
	s_waitcnt vmcnt(7)
	v_lshlrev_b32_e32 v12, 16, v232
	v_and_b32_e32 v13, 0xffff0000, v232
	v_lshlrev_b32_e32 v4, 16, v230
	v_and_b32_e32 v5, 0xffff0000, v230
	v_lshlrev_b32_e32 v6, 16, v231
	v_and_b32_e32 v7, 0xffff0000, v231
	v_pk_fma_f32 v[6:7], v[46:47], v[74:75], v[6:7]
	v_pk_fma_f32 v[4:5], v[44:45], v[72:73], v[4:5]
	v_lshlrev_b32_e32 v14, 16, v233
	v_and_b32_e32 v15, 0xffff0000, v233
	v_pk_fma_f32 v[14:15], v[50:51], v[70:71], v[14:15]
	v_pk_fma_f32 v[12:13], v[48:49], v[68:69], v[12:13]
	v_cvt_pk_bf16_f32 v4, v4, v5
	v_cvt_pk_bf16_f32 v5, v6, v7
	s_nop 0
	v_cvt_pk_bf16_f32 v6, v12, v13
	v_cvt_pk_bf16_f32 v7, v14, v15
	global_store_dwordx4 v[190:191], v[4:7], off offset:256
	s_waitcnt vmcnt(7)
	v_lshlrev_b32_e32 v12, 16, v18
	v_and_b32_e32 v13, 0xffff0000, v18
	v_lshlrev_b32_e32 v4, 16, v16
	v_and_b32_e32 v5, 0xffff0000, v16
	v_lshlrev_b32_e32 v6, 16, v17
	v_and_b32_e32 v7, 0xffff0000, v17
	v_pk_fma_f32 v[6:7], v[46:47], v[66:67], v[6:7]
	v_pk_fma_f32 v[4:5], v[44:45], v[64:65], v[4:5]
	v_lshlrev_b32_e32 v14, 16, v19
	v_and_b32_e32 v15, 0xffff0000, v19
	v_pk_fma_f32 v[14:15], v[50:51], v[62:63], v[14:15]
	v_pk_fma_f32 v[12:13], v[48:49], v[60:61], v[12:13]
	v_cvt_pk_bf16_f32 v4, v4, v5
	v_cvt_pk_bf16_f32 v5, v6, v7
	s_nop 0
	v_cvt_pk_bf16_f32 v6, v12, v13
	v_cvt_pk_bf16_f32 v7, v14, v15
	global_store_dwordx4 v[186:187], v[4:7], off offset:256
	s_waitcnt vmcnt(7)
	s_nop 0
	v_lshlrev_b32_e32 v4, 16, v8
	v_and_b32_e32 v5, 0xffff0000, v8
	v_lshlrev_b32_e32 v6, 16, v9
	v_and_b32_e32 v7, 0xffff0000, v9
	v_pk_fma_f32 v[6:7], v[46:47], v[58:59], v[6:7]
	v_pk_fma_f32 v[4:5], v[44:45], v[56:57], v[4:5]
	v_lshlrev_b32_e32 v8, 16, v10
	v_and_b32_e32 v9, 0xffff0000, v10
	v_lshlrev_b32_e32 v10, 16, v11
	v_and_b32_e32 v11, 0xffff0000, v11
	v_pk_fma_f32 v[10:11], v[50:51], v[54:55], v[10:11]
	v_pk_fma_f32 v[8:9], v[48:49], v[52:53], v[8:9]
	v_cvt_pk_bf16_f32 v4, v4, v5
	v_cvt_pk_bf16_f32 v5, v6, v7
	s_nop 0
	v_cvt_pk_bf16_f32 v6, v8, v9
	v_cvt_pk_bf16_f32 v7, v10, v11
	global_store_dwordx4 v[34:35], v[4:7], off offset:256
	s_cbranch_execz .LBB0_1021

.LBB0_1263:
	s_or_b64 exec, exec, s[2:3]
	s_nop 11
	v_cndmask_b32_e64 v2, 0, 1, s[12:13]
	v_cmp_ne_u32_e64 s[40:41], 1, v2
	s_andn2_b64 vcc, exec, s[12:13]
	s_cbranch_vccnz .LBB0_1265
	s_add_i32 s2, s17, s14
	s_ashr_i32 s3, s2, 31
	s_lshl_b64 s[2:3], s[2:3], 13
	s_add_u32 s12, s20, s2
	s_addc_u32 s13, s21, s3
	s_lshl_b32 s2, s25, 8
	s_ashr_i32 s3, s2, 31
	v_mov_b32_e32 v2, v0
	s_lshl_b64 s[2:3], s[2:3], 2
	s_add_u32 s2, s12, s2
	v_lshlrev_b32_e32 v6, 1, v2
	s_addc_u32 s3, s13, s3
	v_and_b32_e32 v2, 0x180, v6
	v_lshl_add_u64 v[4:5], s[2:3], 0, v[2:3]
	v_and_b32_e32 v2, 0x60, v6
	v_lshl_add_u64 v[4:5], v[4:5], 0, v[2:3]
	global_load_dwordx4 v[36:39], v[4:5], off offset:16
	global_load_dwordx4 v[40:43], v[4:5], off
	global_load_dwordx4 v[44:47], v[4:5], off offset:528
	global_load_dwordx4 v[48:51], v[4:5], off offset:512

.LBB0_1402:
	s_or_b64 exec, exec, s[2:3]
	s_nop 11
	v_cndmask_b32_e64 v2, 0, 1, s[10:11]
	v_cmp_ne_u32_e64 s[40:41], 1, v2
	s_andn2_b64 vcc, exec, s[10:11]
	s_cbranch_vccnz .LBB0_1404
	s_add_i32 s2, s15, s17
	s_ashr_i32 s3, s2, 31
	s_lshl_b64 s[2:3], s[2:3], 12
	s_add_u32 s10, s8, s2
	s_addc_u32 s11, s9, s3
	s_lshl_b32 s2, s19, 8
	s_ashr_i32 s3, s2, 31
	v_mov_b32_e32 v2, v0
	s_lshl_b64 s[2:3], s[2:3], 2
	s_add_u32 s2, s10, s2
	v_lshlrev_b32_e32 v6, 1, v2
	s_addc_u32 s3, s11, s3
	v_and_b32_e32 v2, 0x180, v6
	v_lshl_add_u64 v[4:5], s[2:3], 0, v[2:3]
	v_and_b32_e32 v2, 0x60, v6
	v_lshl_add_u64 v[4:5], v[4:5], 0, v[2:3]
	global_load_dwordx4 v[192:195], v[4:5], off offset:16
	global_load_dwordx4 v[246:249], v[4:5], off
	global_load_dwordx4 v[44:47], v[4:5], off offset:528
	global_load_dwordx4 v[48:51], v[4:5], off offset:512
